# v036 + topk unmono() in 2 VALU (v_ashrrev + v_bitop3 0x93 with mask&0x7fffffff constants) at 37 sites, incl. the separate v_and form
# speedup vs baseline: 1.0045x; 1.0045x over previous
; #define LAS __attribute__((address_space(3)))
; __device__ __forceinline__ f32x4 mfma16(bf16x8 a, bf16x8 b, f32x4 c) { return __builtin_amdgcn_mfma_f32_16x16x32_bf16(a, b, c, 0, 0, 0); }
; __device__ __forceinline__ void topk_phase(LAS unsigned char* lds, const bf16_t* qp, const bf16_t* keys, const float* SU, const float* SV, int* sel_e, float* sel_g, float* sel_su, int G, int b) {
;     ...
;         const int tt = gu.pm * 2 + (ui & 1), h = gu.pn;
;         const int tok = tt * 128 + wid * 16 + fr;
;         if ((ui & 1) == 0) {
;             if (ui == 0) {
;                 const bf16_t* src = keys + (size_t)h * 2 * 16384 + (size_t)krow * 128 + khf * 64;
; #pragma unroll
;                 for (int q8 = 0; q8 < 8; ++q8) kpre[q8] = *(const u32x4*)(src + q8 * 8);
;             } else __syncthreads();
;             LAS bf16_t* dst = KL + krow * 136 + khf * 64;
; #pragma unroll
;             for (int q8 = 0; q8 < 8; ++q8) *(LAS u32x4*)(dst + q8 * 8) = kpre[q8];
;             __syncthreads();
;         } else {
;             pg8::Unit gn;
;             if (SO.next((ui + 1) >> 1, gn)) { const bf16_t* src = keys + (size_t)gn.pn * 2 * 16384 + (size_t)krow * 128 + khf * 64;
; #pragma unroll
;                 for (int q8 = 0; q8 < 8; ++q8) kpre[q8] = *(const u32x4*)(src + q8 * 8); }
;         }
;         unsigned T[2][16];
; #pragma unroll
;         for (int p = 0; p < 2; ++p) {
;             f32x4 acc[8];
; #pragma unroll
;             for (int mt = 0; mt < 8; ++mt) acc[mt] = (f32x4){0.f, 0.f, 0.f, 0.f};
;             bf16x8 bq[4];
; #pragma unroll
;             for (int ks = 0; ks < 4; ++ks) bq[ks] = *(const bf16x8*)(qp + (size_t)tok * D_ + h * 256 + p * 128 + ks * 32 + fq * 8);
;             const LAS bf16_t* kb = KL + p * 128 * 136;
; #pragma unroll
;             for (int mt = 0; mt < 8; ++mt)
; #pragma unroll
;                 for (int ks = 0; ks < 4; ++ks) { const bf16x8 a = *(const LAS bf16x8*)(kb + (mt * 16 + fr) * 136 + ks * 32 + fq * 8); acc[mt] = mfma16(a, bq[ks], acc[mt]); }
.LBB0_659:
	s_and_b32 s0, s52, 1
	s_lshl_b32 s1, s64, 8
	s_lshl_b32 s0, s0, 7
	s_or_b32 s0, s1, s0
	v_add_u32_e32 v94, s0, v85
	v_ashrrev_i32_e32 v95, 31, v94
	v_lshlrev_b64 v[34:35], 12, v[94:95]
	s_lshl_b32 s0, s56, 8
	v_lshl_add_u64 v[34:35], s[74:75], 0, v[34:35]
	s_ashr_i32 s1, s0, 31
	v_lshl_add_u64 v[34:35], s[0:1], 1, v[34:35]
	v_lshl_add_u64 v[96:97], v[34:35], 0, v[78:79]
	global_load_dwordx4 v[66:69], v[96:97], off
	global_load_dwordx4 v[62:65], v[96:97], off offset:64
	global_load_dwordx4 v[58:61], v[96:97], off offset:128
	global_load_dwordx4 v[54:57], v[96:97], off offset:192
	v_add_u32_e32 v138, v87, v89
	ds_read_b128 v[34:37], v138 offset:32768
	ds_read_b128 v[38:41], v138 offset:32832
	s_movk_i32 s0, 0xff
	s_waitcnt vmcnt(3) lgkmcnt(1)
	v_mfma_f32_16x16x32_bf16 v[34:37], v[34:37], v[66:69], 0
	ds_read_b128 v[42:45], v138 offset:41536
	ds_read_b128 v[50:53], v138 offset:45888
	ds_read_b128 v[70:73], v138 offset:50240
	s_waitcnt vmcnt(2) lgkmcnt(3)
	v_mfma_f32_16x16x32_bf16 v[34:37], v[38:41], v[62:65], v[34:37]
	ds_read_b128 v[38:41], v138 offset:32896
	ds_read_b128 v[74:77], v138 offset:54592
	ds_read_b128 v[134:137], v138 offset:58944
	s_waitcnt vmcnt(1) lgkmcnt(2)
	v_mfma_f32_16x16x32_bf16 v[34:37], v[38:41], v[58:61], v[34:37]
	ds_read_b128 v[38:41], v138 offset:32960
	s_waitcnt vmcnt(0) lgkmcnt(0)
	v_mfma_f32_16x16x32_bf16 v[46:49], v[38:41], v[54:57], v[34:37]
	s_nop 4
	ds_read_b128 v[34:37], v138 offset:37120
	ds_read_b128 v[38:41], v138 offset:37184
	s_nop 0
	s_waitcnt lgkmcnt(1)
	v_mfma_f32_16x16x32_bf16 v[34:37], v[34:37], v[66:69], 0
	s_waitcnt lgkmcnt(0)
	v_mfma_f32_16x16x32_bf16 v[34:37], v[38:41], v[62:65], v[34:37]
	ds_read_b128 v[38:41], v138 offset:37248
	s_waitcnt lgkmcnt(0)
	v_mfma_f32_16x16x32_bf16 v[34:37], v[38:41], v[58:61], v[34:37]
	ds_read_b128 v[38:41], v138 offset:37312
	s_waitcnt lgkmcnt(0)
	v_mfma_f32_16x16x32_bf16 v[34:37], v[38:41], v[54:57], v[34:37]
	ds_read_b128 v[38:41], v138 offset:41472
	s_waitcnt lgkmcnt(0)
	v_mfma_f32_16x16x32_bf16 v[38:41], v[38:41], v[66:69], 0
	v_mfma_f32_16x16x32_bf16 v[38:41], v[42:45], v[62:65], v[38:41]
	ds_read_b128 v[42:45], v138 offset:41600
	s_waitcnt lgkmcnt(0)
	v_mfma_f32_16x16x32_bf16 v[38:41], v[42:45], v[58:61], v[38:41]
	ds_read_b128 v[42:45], v138 offset:41664
	s_waitcnt lgkmcnt(0)
	v_mfma_f32_16x16x32_bf16 v[38:41], v[42:45], v[54:57], v[38:41]
	ds_read_b128 v[42:45], v138 offset:45824
	s_waitcnt lgkmcnt(0)
	v_mfma_f32_16x16x32_bf16 v[42:45], v[42:45], v[66:69], 0
	v_mfma_f32_16x16x32_bf16 v[42:45], v[50:53], v[62:65], v[42:45]
	ds_read_b128 v[50:53], v138 offset:45952
	s_waitcnt lgkmcnt(0)
	v_mfma_f32_16x16x32_bf16 v[42:45], v[50:53], v[58:61], v[42:45]
	ds_read_b128 v[50:53], v138 offset:46016
	s_waitcnt lgkmcnt(0)
	v_mfma_f32_16x16x32_bf16 v[42:45], v[50:53], v[54:57], v[42:45]
	ds_read_b128 v[50:53], v138 offset:50176
	s_waitcnt lgkmcnt(0)
	v_mfma_f32_16x16x32_bf16 v[50:53], v[50:53], v[66:69], 0
	v_mfma_f32_16x16x32_bf16 v[50:53], v[70:73], v[62:65], v[50:53]
	ds_read_b128 v[70:73], v138 offset:50304
	s_waitcnt lgkmcnt(0)
	v_mfma_f32_16x16x32_bf16 v[50:53], v[70:73], v[58:61], v[50:53]
	ds_read_b128 v[70:73], v138 offset:50368
	s_waitcnt lgkmcnt(0)
	v_mfma_f32_16x16x32_bf16 v[70:73], v[70:73], v[54:57], v[50:53]
	s_nop 4
	ds_read_b128 v[50:53], v138 offset:54528
	s_waitcnt lgkmcnt(0)
	v_mfma_f32_16x16x32_bf16 v[50:53], v[50:53], v[66:69], 0
	v_mfma_f32_16x16x32_bf16 v[50:53], v[74:77], v[62:65], v[50:53]
	ds_read_b128 v[74:77], v138 offset:54656
	s_waitcnt lgkmcnt(0)
	v_mfma_f32_16x16x32_bf16 v[50:53], v[74:77], v[58:61], v[50:53]
	ds_read_b128 v[74:77], v138 offset:54720
	s_waitcnt lgkmcnt(0)
	v_mfma_f32_16x16x32_bf16 v[50:53], v[74:77], v[54:57], v[50:53]
	ds_read_b128 v[74:77], v138 offset:58880
	s_waitcnt lgkmcnt(0)
	v_mfma_f32_16x16x32_bf16 v[74:77], v[74:77], v[66:69], 0
	v_mfma_f32_16x16x32_bf16 v[74:77], v[134:137], v[62:65], v[74:77]
	ds_read_b128 v[134:137], v138 offset:59008
	s_waitcnt lgkmcnt(0)
	v_mfma_f32_16x16x32_bf16 v[74:77], v[134:137], v[58:61], v[74:77]
	ds_read_b128 v[134:137], v138 offset:59072
	s_waitcnt lgkmcnt(0)
	v_mfma_f32_16x16x32_bf16 v[74:77], v[134:137], v[54:57], v[74:77]
	ds_read_b128 v[134:137], v138 offset:63232
	s_waitcnt lgkmcnt(0)
	v_mfma_f32_16x16x32_bf16 v[66:69], v[134:137], v[66:69], 0
	ds_read_b128 v[134:137], v138 offset:63296
	s_waitcnt lgkmcnt(0)
	v_mfma_f32_16x16x32_bf16 v[62:65], v[134:137], v[62:65], v[66:69]
	s_nop 4
	ds_read_b128 v[66:69], v138 offset:63360
	s_waitcnt lgkmcnt(0)
	v_mfma_f32_16x16x32_bf16 v[58:61], v[66:69], v[58:61], v[62:65]
	s_nop 2
	ds_read_b128 v[62:65], v138 offset:63424
	s_waitcnt lgkmcnt(0)
; __device__ __forceinline__ unsigned mono(float f) { const unsigned u = __float_as_uint(f); return (u & 0x80000000u) ? ~u : (u ^ 0x80000000u); }
; __device__ __forceinline__ void topk_phase(LAS unsigned char* lds, const bf16_t* qp, const bf16_t* keys, const float* SU, const float* SV, int* sel_e, float* sel_g, float* sel_su, int G, int b) {
;     ...
;             unsigned lo16[16];
; #pragma unroll
;             for (int mt = 0; mt < 4; ++mt)
; #pragma unroll
;                 for (int r = 0; r < 4; ++r) {
;                     T[p][mt * 4 + r] = (mono(acc[mt][r]) & ~127u) | (unsigned)(127 - (mt * 16 + fq * 4 + r));
;                     lo16[mt * 4 + r] = (mono(acc[mt + 4][r]) & ~127u) | (unsigned)(127 - ((mt + 4) * 16 + fq * 4 + r));
;                 }
;             SN_SORT16(T[p]); SN_SORT16(lo16);
	v_mfma_f32_16x16x32_bf16 v[54:57], v[62:65], v[54:57], v[58:61]
	s_nop 2
	v_ashrrev_i32_e32 v58, 31, v46
	v_bitop3_b32 v46, v46, v58, v132 bitop3:0x1e
	v_and_or_b32 v46, v46, s53, v98
	v_ashrrev_i32_e32 v58, 31, v70
	v_bitop3_b32 v58, v70, v58, v132 bitop3:0x1e
	v_and_or_b32 v58, v58, s53, v99
	v_ashrrev_i32_e32 v59, 31, v47
	v_bitop3_b32 v47, v47, v59, v132 bitop3:0x1e
	v_and_or_b32 v47, v47, s53, v100
	v_ashrrev_i32_e32 v59, 31, v71
	v_bitop3_b32 v59, v71, v59, v132 bitop3:0x1e
	v_and_or_b32 v59, v59, s53, v101
	v_ashrrev_i32_e32 v60, 31, v48
	v_bitop3_b32 v48, v48, v60, v132 bitop3:0x1e
	v_and_or_b32 v48, v48, s53, v102
	v_ashrrev_i32_e32 v60, 31, v72
	v_bitop3_b32 v60, v72, v60, v132 bitop3:0x1e
	v_and_or_b32 v60, v60, s53, v103
	v_ashrrev_i32_e32 v61, 31, v49
	v_bitop3_b32 v49, v49, v61, v132 bitop3:0x1e
	v_and_or_b32 v49, v49, s53, v104
	v_ashrrev_i32_e32 v61, 31, v73
	v_bitop3_b32 v61, v73, v61, v132 bitop3:0x1e
	v_and_or_b32 v61, v61, s53, v105
	v_ashrrev_i32_e32 v62, 31, v34
	v_bitop3_b32 v34, v34, v62, v132 bitop3:0x1e
	v_and_or_b32 v34, v34, s53, v106
	v_ashrrev_i32_e32 v62, 31, v50
	v_bitop3_b32 v50, v50, v62, v132 bitop3:0x1e
	v_and_or_b32 v50, v50, s53, v107
	v_ashrrev_i32_e32 v62, 31, v35
	v_bitop3_b32 v35, v35, v62, v132 bitop3:0x1e
	v_and_or_b32 v35, v35, s53, v108
	v_ashrrev_i32_e32 v62, 31, v51
	v_bitop3_b32 v51, v51, v62, v132 bitop3:0x1e
	v_and_or_b32 v51, v51, s53, v109
	v_ashrrev_i32_e32 v62, 31, v36
	v_bitop3_b32 v36, v36, v62, v132 bitop3:0x1e
	v_and_or_b32 v36, v36, s53, v110
	v_ashrrev_i32_e32 v62, 31, v52
	v_bitop3_b32 v52, v52, v62, v132 bitop3:0x1e
	v_and_or_b32 v52, v52, s53, v111
	v_ashrrev_i32_e32 v62, 31, v37
	v_bitop3_b32 v37, v37, v62, v132 bitop3:0x1e
	v_and_or_b32 v37, v37, s53, v112
	v_ashrrev_i32_e32 v62, 31, v53
	v_bitop3_b32 v53, v53, v62, v132 bitop3:0x1e
	v_and_or_b32 v53, v53, s53, v113
	v_ashrrev_i32_e32 v62, 31, v38
	v_bitop3_b32 v38, v38, v62, v132 bitop3:0x1e
	v_and_or_b32 v38, v38, s53, v114
	v_ashrrev_i32_e32 v62, 31, v74
	v_bitop3_b32 v62, v74, v62, v132 bitop3:0x1e
	v_max_u32_e32 v74, v58, v59
	v_ashrrev_i32_e32 v63, 31, v39
	v_cmp_lt_i32_e32 vcc, -1, v75
	v_bitop3_b32 v39, v39, v63, v132 bitop3:0x1e
	v_min_u32_e32 v58, v58, v59
	v_cndmask_b32_e32 v63, -1, v132, vcc
	v_max_u32_e32 v59, v60, v61
	v_min_u32_e32 v60, v60, v61
	v_ashrrev_i32_e32 v64, 31, v40
	v_cmp_lt_i32_e32 vcc, -1, v76
	v_bitop3_b32 v40, v40, v64, v132 bitop3:0x1e
	v_max_u32_e32 v61, v74, v59
	v_cndmask_b32_e32 v64, -1, v132, vcc
	v_min_u32_e32 v59, v74, v59
	v_max_u32_e32 v74, v58, v60
	v_ashrrev_i32_e32 v65, 31, v41
	v_cmp_lt_i32_e32 vcc, -1, v77
	v_bitop3_b32 v41, v41, v65, v132 bitop3:0x1e
	v_min_u32_e32 v58, v58, v60
	v_cndmask_b32_e32 v65, -1, v132, vcc
	v_max_u32_e32 v60, v74, v59
	v_min_u32_e32 v59, v74, v59
	v_ashrrev_i32_e32 v66, 31, v42
	v_bitop3_b32 v42, v42, v66, v132 bitop3:0x1e
	v_max_u32_e32 v74, v50, v51
	v_ashrrev_i32_e32 v66, 31, v54
	v_bitop3_b32 v54, v54, v66, v132 bitop3:0x1e
	v_min_u32_e32 v50, v50, v51
	v_ashrrev_i32_e32 v66, 31, v43
	v_bitop3_b32 v43, v43, v66, v132 bitop3:0x1e
	v_max_u32_e32 v51, v52, v53
	v_ashrrev_i32_e32 v66, 31, v55
	v_bitop3_b32 v55, v55, v66, v132 bitop3:0x1e
	v_min_u32_e32 v52, v52, v53
	v_ashrrev_i32_e32 v66, 31, v44
	v_bitop3_b32 v44, v44, v66, v132 bitop3:0x1e
	v_max_u32_e32 v53, v74, v51
	v_ashrrev_i32_e32 v66, 31, v56
	v_bitop3_b32 v56, v56, v66, v132 bitop3:0x1e
	v_min_u32_e32 v51, v74, v51
	v_ashrrev_i32_e32 v66, 31, v45
	v_cmp_lt_i32_e32 vcc, -1, v57
	v_bitop3_b32 v45, v45, v66, v132 bitop3:0x1e
	v_max_u32_e32 v74, v50, v52
	v_cndmask_b32_e32 v66, -1, v132, vcc
	v_xor_b32_e32 v57, v66, v57
	v_max_u32_e32 v66, v46, v47
	v_min_u32_e32 v46, v46, v47
	v_max_u32_e32 v47, v48, v49
	v_min_u32_e32 v48, v48, v49
	v_max_u32_e32 v49, v66, v47
	v_min_u32_e32 v47, v66, v47
	v_max_u32_e32 v66, v46, v48
	v_min_u32_e32 v46, v46, v48
	v_max_u32_e32 v48, v66, v47
	v_min_u32_e32 v47, v66, v47
	v_max_u32_e32 v66, v34, v35
	v_min_u32_e32 v34, v34, v35
	v_max_u32_e32 v35, v36, v37
	v_min_u32_e32 v36, v36, v37
	v_max_u32_e32 v37, v66, v35
	v_min_u32_e32 v35, v66, v35
	v_max_u32_e32 v66, v34, v36
	v_min_u32_e32 v34, v34, v36
	v_max_u32_e32 v36, v66, v35
	v_min_u32_e32 v35, v66, v35
	v_min_u32_e32 v50, v50, v52
	v_max_u32_e32 v52, v74, v51
	v_min_u32_e32 v51, v74, v51
	v_max_u32_e32 v66, v49, v37
	v_min_u32_e32 v37, v49, v37
	v_max_u32_e32 v49, v47, v35
	v_max_u32_e32 v74, v61, v53
	v_min_u32_e32 v53, v61, v53
	v_max_u32_e32 v61, v59, v51
	v_xor_b32_e32 v63, v63, v75
	v_xor_b32_e32 v64, v64, v76
	v_xor_b32_e32 v65, v65, v77
	v_min_u32_e32 v35, v47, v35
	v_max_u32_e32 v47, v49, v37
	v_min_u32_e32 v37, v49, v37
	v_max_u32_e32 v49, v48, v36
	v_min_u32_e32 v36, v48, v36
	v_max_u32_e32 v48, v46, v34
	v_min_u32_e32 v51, v59, v51
	v_max_u32_e32 v59, v61, v53
	v_min_u32_e32 v53, v61, v53
	v_max_u32_e32 v61, v60, v52
	v_min_u32_e32 v52, v60, v52
	v_max_u32_e32 v60, v58, v50
	v_and_or_b32 v62, v62, s53, v115
	v_and_or_b32 v39, v39, s53, v116
	v_and_or_b32 v63, v63, s53, v117
	v_and_or_b32 v40, v40, s53, v118
	v_and_or_b32 v64, v64, s53, v119
	v_and_or_b32 v41, v41, s53, v120
	v_and_or_b32 v65, v65, s53, v121
	v_min_u32_e32 v34, v46, v34
	v_max_u32_e32 v46, v48, v36
	v_min_u32_e32 v36, v48, v36
	v_min_u32_e32 v50, v58, v50
	v_max_u32_e32 v58, v60, v52
	v_min_u32_e32 v52, v60, v52
	v_max_u32_e32 v48, v49, v47
	v_min_u32_e32 v47, v49, v47
	v_max_u32_e32 v49, v46, v37
	v_min_u32_e32 v37, v46, v37
	v_max_u32_e32 v46, v36, v35
	v_min_u32_e32 v35, v36, v35
	v_max_u32_e32 v36, v38, v39
	v_min_u32_e32 v38, v38, v39
	v_max_u32_e32 v39, v40, v41
	v_min_u32_e32 v40, v40, v41
	v_max_u32_e32 v60, v61, v59
; __device__ __forceinline__ void topk_phase(LAS unsigned char* lds, const bf16_t* qp, const bf16_t* keys, const float* SU, const float* SV, int* sel_e, float* sel_g, float* sel_su, int G, int b) {
;     ...
;             SN_SORT16(T[p]); SN_SORT16(lo16);
; #pragma unroll
;             for (int i = 0; i < 16; ++i) T[p][i] = umax_(T[p][i], lo16[15 - i]);
;             SN_BITONIC16(T[p]);
	v_min_u32_e32 v59, v61, v59
	v_max_u32_e32 v61, v58, v53
	v_min_u32_e32 v53, v58, v53
	v_max_u32_e32 v58, v52, v51
	v_min_u32_e32 v51, v52, v51
	v_max_u32_e32 v52, v62, v63
	v_min_u32_e32 v62, v62, v63
	v_max_u32_e32 v63, v64, v65
	v_min_u32_e32 v64, v64, v65
	v_and_or_b32 v42, v42, s53, v122
	v_and_or_b32 v54, v54, s53, v123
	v_and_or_b32 v43, v43, s53, v124
	v_and_or_b32 v55, v55, s53, v125
	v_and_or_b32 v44, v44, s53, v126
	v_and_or_b32 v56, v56, s53, v127
	v_and_or_b32 v45, v45, s53, v128
	v_and_or_b32 v57, v57, s53, v129
	v_max_u32_e32 v41, v36, v39
	v_min_u32_e32 v36, v36, v39
	v_max_u32_e32 v39, v38, v40
	v_max_u32_e32 v65, v52, v63
	v_min_u32_e32 v52, v52, v63
	v_max_u32_e32 v63, v62, v64
	v_min_u32_e32 v38, v38, v40
	v_max_u32_e32 v40, v39, v36
	v_min_u32_e32 v36, v39, v36
	v_max_u32_e32 v39, v42, v43
	v_min_u32_e32 v42, v42, v43
	v_max_u32_e32 v43, v44, v45
	v_min_u32_e32 v44, v44, v45
	v_min_u32_e32 v62, v62, v64
	v_max_u32_e32 v64, v63, v52
	v_min_u32_e32 v52, v63, v52
	v_max_u32_e32 v63, v54, v55
	v_min_u32_e32 v54, v54, v55
	v_max_u32_e32 v55, v56, v57
	v_min_u32_e32 v56, v56, v57
	v_max_u32_e32 v45, v39, v43
	v_min_u32_e32 v39, v39, v43
	v_max_u32_e32 v43, v42, v44
	v_max_u32_e32 v57, v63, v55
	v_min_u32_e32 v55, v63, v55
	v_max_u32_e32 v63, v54, v56
	v_min_u32_e32 v42, v42, v44
	v_max_u32_e32 v44, v43, v39
	v_min_u32_e32 v39, v43, v39
	v_min_u32_e32 v54, v54, v56
	v_max_u32_e32 v56, v63, v55
	v_min_u32_e32 v55, v63, v55
	v_max_u32_e32 v43, v41, v45
	v_min_u32_e32 v41, v41, v45
	v_max_u32_e32 v45, v36, v39
	v_max_u32_e32 v63, v65, v57
	v_min_u32_e32 v57, v65, v57
	v_max_u32_e32 v65, v52, v55
	v_min_u32_e32 v36, v36, v39
	v_max_u32_e32 v39, v45, v41
	v_min_u32_e32 v41, v45, v41
	v_max_u32_e32 v45, v40, v44
	v_min_u32_e32 v40, v40, v44
	v_max_u32_e32 v44, v38, v42
	v_min_u32_e32 v52, v52, v55
	v_max_u32_e32 v55, v65, v57
	v_min_u32_e32 v57, v65, v57
	v_max_u32_e32 v65, v64, v56
	v_min_u32_e32 v56, v64, v56
	v_max_u32_e32 v64, v62, v54
	v_min_u32_e32 v38, v38, v42
	v_max_u32_e32 v42, v44, v40
	v_min_u32_e32 v54, v62, v54
	v_max_u32_e32 v62, v64, v56
	v_min_u32_e32 v40, v44, v40
	v_max_u32_e32 v44, v45, v39
	v_min_u32_e32 v39, v45, v39
	v_max_u32_e32 v45, v42, v41
	v_min_u32_e32 v41, v42, v41
	v_min_u32_e32 v56, v64, v56
	v_max_u32_e32 v64, v65, v55
	v_min_u32_e32 v55, v65, v55
	v_max_u32_e32 v65, v62, v57
	v_min_u32_e32 v57, v62, v57
	v_max_u32_e32 v42, v40, v36
	v_min_u32_e32 v36, v40, v36
	v_min_u32_e32 v40, v66, v43
	v_max_u32_e32 v67, v37, v41
	v_max_u32_e32 v62, v56, v52
	v_min_u32_e32 v52, v56, v52
	v_min_u32_e32 v56, v74, v63
	v_max_u32_e32 v75, v53, v57
	v_min_u32_e32 v37, v37, v41
	v_max_u32_e32 v41, v67, v40
	v_min_u32_e32 v40, v67, v40
	v_max_u32_e32 v67, v47, v39
	v_min_u32_e32 v39, v47, v39
	v_max_u32_e32 v47, v35, v36
	v_min_u32_e32 v53, v53, v57
	v_max_u32_e32 v57, v75, v56
	v_min_u32_e32 v56, v75, v56
	v_max_u32_e32 v75, v59, v55
	v_min_u32_e32 v55, v59, v55
	v_max_u32_e32 v59, v51, v52
	v_min_u32_e32 v35, v35, v36
	v_max_u32_e32 v36, v47, v39
	v_min_u32_e32 v39, v47, v39
	v_min_u32_e32 v51, v51, v52
	v_max_u32_e32 v52, v59, v55
	v_min_u32_e32 v55, v59, v55
	v_max_u32_e32 v47, v67, v41
	v_min_u32_e32 v41, v67, v41
	v_max_u32_e32 v67, v36, v40
	v_min_u32_e32 v36, v36, v40
	v_max_u32_e32 v40, v39, v37
	v_min_u32_e32 v37, v39, v37
	v_max_u32_e32 v39, v48, v44
	v_min_u32_e32 v44, v48, v44
	v_max_u32_e32 v48, v46, v42
	v_max_u32_e32 v59, v75, v57
	v_min_u32_e32 v57, v75, v57
	v_max_u32_e32 v75, v52, v56
	v_min_u32_e32 v52, v52, v56
	v_max_u32_e32 v56, v55, v53
	v_min_u32_e32 v53, v55, v53
	v_max_u32_e32 v55, v60, v64
	v_min_u32_e32 v60, v60, v64
	v_max_u32_e32 v64, v58, v62
	v_min_u32_e32 v42, v46, v42
	v_max_u32_e32 v46, v48, v44
	v_min_u32_e32 v44, v48, v44
	v_max_u32_e32 v48, v49, v45
	v_min_u32_e32 v45, v49, v45
	v_max_u32_e32 v49, v34, v38
	v_min_u32_e32 v58, v58, v62
	v_max_u32_e32 v62, v64, v60
	v_min_u32_e32 v60, v64, v60
	v_max_u32_e32 v64, v61, v65
	v_min_u32_e32 v61, v61, v65
	v_max_u32_e32 v65, v50, v54
	v_min_u32_e32 v34, v34, v38
	v_max_u32_e32 v38, v49, v45
	v_min_u32_e32 v45, v49, v45
	v_min_u32_e32 v50, v50, v54
	v_max_u32_e32 v54, v65, v61
	v_min_u32_e32 v61, v65, v61
	v_max_u32_e32 v49, v48, v46
	v_min_u32_e32 v46, v48, v46
	v_max_u32_e32 v48, v38, v44
	v_min_u32_e32 v38, v38, v44
	v_max_u32_e32 v44, v45, v42
	v_min_u32_e32 v42, v45, v42
	v_max_u32_e32 v65, v64, v62
	v_min_u32_e32 v62, v64, v62
	v_max_u32_e32 v64, v54, v60
	v_min_u32_e32 v54, v54, v60
	v_max_u32_e32 v60, v61, v58
	v_min_u32_e32 v58, v61, v58
	v_min_u32_e32 v45, v39, v47
	v_min_u32_e32 v68, v49, v41
	v_min_u32_e32 v69, v46, v67
	v_min_u32_e32 v70, v48, v36
	v_min_u32_e32 v71, v38, v40
	v_min_u32_e32 v72, v44, v37
	v_min_u32_e32 v73, v42, v35
	v_min_u32_e32 v61, v55, v59
	v_min_u32_e32 v76, v65, v57
	v_min_u32_e32 v77, v62, v75
	v_min_u32_e32 v134, v64, v52
	v_min_u32_e32 v135, v54, v56
	v_min_u32_e32 v136, v60, v53
	v_min_u32_e32 v137, v58, v51
	v_max3_u32 v43, v66, v43, v50
	v_max3_u32 v39, v39, v47, v137
	v_max3_u32 v45, v45, v58, v51
	v_max3_u32 v41, v49, v41, v136
	v_max3_u32 v47, v68, v60, v53
	v_max3_u32 v46, v46, v67, v135
	v_max3_u32 v49, v69, v54, v56
	v_max3_u32 v36, v48, v36, v134
	v_max3_u32 v48, v70, v64, v52
	v_max3_u32 v38, v38, v40, v77
	v_max3_u32 v40, v71, v62, v75
	v_max3_u32 v37, v44, v37, v76
	v_max3_u32 v44, v72, v65, v57
	v_max3_u32 v35, v42, v35, v61
	v_max3_u32 v42, v73, v55, v59
	v_max3_u32 v34, v34, v74, v63
	v_max_u32_e32 v50, v43, v48
	v_min_u32_e32 v43, v43, v48
	v_max_u32_e32 v48, v39, v38
	v_min_u32_e32 v38, v39, v38
	v_max_u32_e32 v39, v45, v40
	v_min_u32_e32 v40, v45, v40
	v_max_u32_e32 v45, v41, v37
; #define LAS __attribute__((address_space(3)))
; __device__ __forceinline__ f32x4 mfma16(bf16x8 a, bf16x8 b, f32x4 c) { return __builtin_amdgcn_mfma_f32_16x16x32_bf16(a, b, c, 0, 0, 0); }
; __device__ __forceinline__ void topk_phase(LAS unsigned char* lds, const bf16_t* qp, const bf16_t* keys, const float* SU, const float* SV, int* sel_e, float* sel_g, float* sel_su, int G, int b) {
;     ...
;             bf16x8 bq[4];
; #pragma unroll
;             for (int ks = 0; ks < 4; ++ks) bq[ks] = *(const bf16x8*)(qp + (size_t)tok * D_ + h * 256 + p * 128 + ks * 32 + fq * 8);
;             const LAS bf16_t* kb = KL + p * 128 * 136;
; #pragma unroll
;             for (int mt = 0; mt < 8; ++mt)
; #pragma unroll
;                 for (int ks = 0; ks < 4; ++ks) { const bf16x8 a = *(const LAS bf16x8*)(kb + (mt * 16 + fr) * 136 + ks * 32 + fq * 8); acc[mt] = mfma16(a, bq[ks], acc[mt]); }
	v_min_u32_e32 v37, v41, v37
	v_max_u32_e32 v41, v47, v44
	v_min_u32_e32 v44, v47, v44
	v_max_u32_e32 v47, v46, v35
	v_min_u32_e32 v35, v46, v35
	v_max_u32_e32 v46, v49, v42
	v_min_u32_e32 v42, v49, v42
	v_max_u32_e32 v49, v36, v34
	v_min_u32_e32 v34, v36, v34
	v_max_u32_e32 v36, v50, v41
	v_min_u32_e32 v41, v50, v41
	v_max_u32_e32 v50, v48, v47
	v_min_u32_e32 v47, v48, v47
	v_max_u32_e32 v48, v39, v46
	v_min_u32_e32 v39, v39, v46
	v_max_u32_e32 v46, v45, v49
	v_min_u32_e32 v45, v45, v49
	v_max_u32_e32 v49, v43, v44
	v_min_u32_e32 v43, v43, v44
	v_max_u32_e32 v44, v38, v35
	v_min_u32_e32 v35, v38, v35
	v_max_u32_e32 v38, v40, v42
	v_min_u32_e32 v40, v40, v42
	v_max_u32_e32 v42, v37, v34
	v_min_u32_e32 v34, v37, v34
	v_max_u32_e32 v37, v36, v48
	v_min_u32_e32 v36, v36, v48
	v_max_u32_e32 v48, v50, v46
	v_min_u32_e32 v46, v50, v46
	v_max_u32_e32 v50, v41, v39
	v_min_u32_e32 v39, v41, v39
	v_max_u32_e32 v41, v47, v45
	v_min_u32_e32 v45, v47, v45
	v_max_u32_e32 v47, v49, v38
	v_min_u32_e32 v38, v49, v38
	v_max_u32_e32 v49, v44, v42
	v_min_u32_e32 v42, v44, v42
	v_max_u32_e32 v44, v43, v40
	v_min_u32_e32 v40, v43, v40
	v_max_u32_e32 v43, v35, v34
	v_min_u32_e32 v34, v35, v34
	v_max_u32_e32 v35, v37, v48
	v_min_u32_e32 v37, v37, v48
	v_max_u32_e32 v48, v36, v46
	v_min_u32_e32 v36, v36, v46
	v_max_u32_e32 v46, v50, v41
	v_min_u32_e32 v41, v50, v41
	v_max_u32_e32 v50, v39, v45
	v_min_u32_e32 v39, v39, v45
	v_max_u32_e32 v45, v47, v49
	v_min_u32_e32 v47, v47, v49
	v_max_u32_e32 v49, v38, v42
	v_min_u32_e32 v38, v38, v42
	v_max_u32_e32 v42, v44, v43
	v_min_u32_e32 v43, v44, v43
	v_max_u32_e32 v44, v40, v34
	v_min_u32_e32 v34, v40, v34
	v_mov_b32_e32 v40, v35
	v_mov_b32_e32 v51, v37
	v_mov_b32_e32 v52, v48
	v_mov_b32_e32 v53, v36
	v_mov_b32_e32 v54, v46
	v_mov_b32_e32 v55, v41
	v_mov_b32_e32 v56, v50
	v_mov_b32_e32 v57, v39
	v_mov_b32_e32 v58, v45
	v_mov_b32_e32 v59, v47
	v_mov_b32_e32 v60, v49
	v_mov_b32_e32 v61, v38
	v_mov_b32_e32 v62, v42
	v_mov_b32_e32 v63, v43
	v_mov_b32_e32 v64, v44
	v_mov_b32_e32 v65, v34
	v_permlane16_swap_b32_e32 v35, v40
	v_permlane16_swap_b32_e32 v37, v51
	v_permlane16_swap_b32_e32 v48, v52
	v_permlane16_swap_b32_e32 v36, v53
	v_permlane16_swap_b32_e32 v46, v54
	v_permlane16_swap_b32_e32 v41, v55
	v_permlane16_swap_b32_e32 v50, v56
	v_permlane16_swap_b32_e32 v39, v57
	v_permlane16_swap_b32_e32 v45, v58
	v_permlane16_swap_b32_e32 v47, v59
	v_permlane16_swap_b32_e32 v49, v60
	v_permlane16_swap_b32_e32 v38, v61
	v_permlane16_swap_b32_e32 v42, v62
	v_permlane16_swap_b32_e32 v43, v63
	v_permlane16_swap_b32_e32 v44, v64
	v_permlane16_swap_b32_e32 v34, v65
	v_max_u32_e32 v35, v35, v65
	v_max_u32_e32 v37, v37, v64
	v_max_u32_e32 v48, v48, v63
	v_max_u32_e32 v36, v36, v62
	v_max_u32_e32 v46, v46, v61
	v_max_u32_e32 v41, v41, v60
	v_max_u32_e32 v50, v50, v59
	v_max_u32_e32 v39, v39, v58
	v_max_u32_e32 v45, v45, v57
	v_max_u32_e32 v47, v47, v56
	v_max_u32_e32 v49, v49, v55
	v_max_u32_e32 v38, v38, v54
	v_max_u32_e32 v42, v42, v53
	v_max_u32_e32 v43, v43, v52
	v_max_u32_e32 v44, v44, v51
	v_max_u32_e32 v34, v34, v40
	v_max_u32_e32 v40, v35, v45
	v_min_u32_e32 v35, v35, v45
	v_max_u32_e32 v45, v37, v47
	v_min_u32_e32 v37, v37, v47
	v_max_u32_e32 v47, v48, v49
	v_min_u32_e32 v48, v48, v49
	v_max_u32_e32 v49, v36, v38
	v_min_u32_e32 v36, v36, v38
	v_max_u32_e32 v38, v46, v42
	v_min_u32_e32 v42, v46, v42
	v_max_u32_e32 v46, v41, v43
	v_min_u32_e32 v41, v41, v43
	v_max_u32_e32 v43, v50, v44
	v_min_u32_e32 v44, v50, v44
	v_max_u32_e32 v50, v39, v34
	v_min_u32_e32 v34, v39, v34
	v_max_u32_e32 v39, v40, v38
	v_min_u32_e32 v38, v40, v38
	v_max_u32_e32 v40, v45, v46
	v_min_u32_e32 v45, v45, v46
	v_max_u32_e32 v46, v47, v43
	v_min_u32_e32 v43, v47, v43
	v_max_u32_e32 v47, v49, v50
	v_min_u32_e32 v49, v49, v50
	v_max_u32_e32 v50, v35, v42
	v_min_u32_e32 v35, v35, v42
	v_max_u32_e32 v42, v37, v41
	v_min_u32_e32 v37, v37, v41
	v_max_u32_e32 v41, v48, v44
	v_min_u32_e32 v44, v48, v44
	v_max_u32_e32 v48, v36, v34
	v_min_u32_e32 v34, v36, v34
	v_max_u32_e32 v36, v39, v46
	v_min_u32_e32 v39, v39, v46
	v_max_u32_e32 v46, v40, v47
	v_min_u32_e32 v40, v40, v47
	v_max_u32_e32 v47, v38, v43
	v_min_u32_e32 v38, v38, v43
	v_max_u32_e32 v43, v45, v49
	v_min_u32_e32 v45, v45, v49
	v_max_u32_e32 v49, v50, v41
	v_min_u32_e32 v41, v50, v41
	v_max_u32_e32 v50, v42, v48
	v_min_u32_e32 v42, v42, v48
	v_max_u32_e32 v48, v35, v44
	v_min_u32_e32 v35, v35, v44
	v_max_u32_e32 v44, v37, v34
	v_min_u32_e32 v34, v37, v34
	v_max_u32_e32 v70, v36, v46
	v_min_u32_e32 v71, v36, v46
	v_max_u32_e32 v72, v39, v40
	v_min_u32_e32 v73, v39, v40
	v_max_u32_e32 v74, v47, v43
	v_min_u32_e32 v75, v47, v43
	v_max_u32_e32 v76, v38, v45
	v_min_u32_e32 v77, v38, v45
	v_max_u32_e32 v134, v49, v50
	v_min_u32_e32 v135, v49, v50
	v_max_u32_e32 v136, v41, v42
	v_min_u32_e32 v137, v41, v42
	v_max_u32_e32 v138, v48, v44
	v_min_u32_e32 v139, v48, v44
	v_max_u32_e32 v140, v35, v34
	v_min_u32_e32 v141, v35, v34
	global_load_dwordx4 v[46:49], v[96:97], off offset:256
	global_load_dwordx4 v[42:45], v[96:97], off offset:320
	global_load_dwordx4 v[38:41], v[96:97], off offset:384
	global_load_dwordx4 v[34:37], v[96:97], off offset:448
	ds_read_b128 v[50:53], v131 offset:34816
	ds_read_b128 v[54:57], v131 offset:34880
	s_waitcnt vmcnt(3) lgkmcnt(1)
	v_mfma_f32_16x16x32_bf16 v[50:53], v[50:53], v[46:49], 0
	ds_read_b128 v[58:61], v131 offset:39232
	ds_read_b128 v[62:65], v131 offset:43584
	ds_read_b128 v[66:69], v131 offset:47936
	s_waitcnt vmcnt(2) lgkmcnt(3)
	v_mfma_f32_16x16x32_bf16 v[50:53], v[54:57], v[42:45], v[50:53]
	ds_read_b128 v[54:57], v131 offset:34944
	ds_read_b128 v[158:161], v131 offset:52288
	ds_read_b128 v[162:165], v131 offset:56640
	s_waitcnt vmcnt(1) lgkmcnt(2)
; #define LAS __attribute__((address_space(3)))
; __device__ __forceinline__ f32x4 mfma16(bf16x8 a, bf16x8 b, f32x4 c) { return __builtin_amdgcn_mfma_f32_16x16x32_bf16(a, b, c, 0, 0, 0); }
; __device__ __forceinline__ void topk_phase(LAS unsigned char* lds, const bf16_t* qp, const bf16_t* keys, const float* SU, const float* SV, int* sel_e, float* sel_g, float* sel_su, int G, int b) {
;     ...
;             bf16x8 bq[4];
; #pragma unroll
;             for (int ks = 0; ks < 4; ++ks) bq[ks] = *(const bf16x8*)(qp + (size_t)tok * D_ + h * 256 + p * 128 + ks * 32 + fq * 8);
;             const LAS bf16_t* kb = KL + p * 128 * 136;
; #pragma unroll
;             for (int mt = 0; mt < 8; ++mt)
; #pragma unroll
;                 for (int ks = 0; ks < 4; ++ks) { const bf16x8 a = *(const LAS bf16x8*)(kb + (mt * 16 + fr) * 136 + ks * 32 + fq * 8); acc[mt] = mfma16(a, bq[ks], acc[mt]); }
	v_mfma_f32_16x16x32_bf16 v[50:53], v[54:57], v[38:41], v[50:53]
	ds_read_b128 v[54:57], v131 offset:35008
	ds_read_b128 v[166:169], v131 offset:60992
	v_mov_b32_e32 v142, v70
	s_waitcnt vmcnt(0) lgkmcnt(1)
	v_mfma_f32_16x16x32_bf16 v[50:53], v[54:57], v[34:37], v[50:53]
	ds_read_b128 v[54:57], v131 offset:39168
	v_mov_b32_e32 v143, v71
	v_mov_b32_e32 v144, v72
	s_waitcnt lgkmcnt(0)
	v_mfma_f32_16x16x32_bf16 v[54:57], v[54:57], v[46:49], 0
	s_nop 2
	v_mov_b32_e32 v145, v73
	v_mov_b32_e32 v146, v74
	v_mfma_f32_16x16x32_bf16 v[54:57], v[58:61], v[42:45], v[54:57]
	ds_read_b128 v[58:61], v131 offset:39296
	v_mov_b32_e32 v147, v75
	v_mov_b32_e32 v148, v76
	s_waitcnt lgkmcnt(0)
	v_mfma_f32_16x16x32_bf16 v[54:57], v[58:61], v[38:41], v[54:57]
	ds_read_b128 v[58:61], v131 offset:39360
	v_mov_b32_e32 v149, v77
	v_mov_b32_e32 v150, v134
	s_waitcnt lgkmcnt(0)
	v_mfma_f32_16x16x32_bf16 v[54:57], v[58:61], v[34:37], v[54:57]
	ds_read_b128 v[58:61], v131 offset:43520
	v_mov_b32_e32 v151, v135
	v_mov_b32_e32 v152, v136
	s_waitcnt lgkmcnt(0)
	v_mfma_f32_16x16x32_bf16 v[58:61], v[58:61], v[46:49], 0
	v_mov_b32_e32 v153, v137
	v_mov_b32_e32 v154, v138
	v_mov_b32_e32 v155, v139
	v_mfma_f32_16x16x32_bf16 v[58:61], v[62:65], v[42:45], v[58:61]
	ds_read_b128 v[62:65], v131 offset:43648
	v_mov_b32_e32 v156, v140
	v_mov_b32_e32 v157, v141
	s_waitcnt lgkmcnt(0)
	v_mfma_f32_16x16x32_bf16 v[58:61], v[62:65], v[38:41], v[58:61]
	ds_read_b128 v[62:65], v131 offset:43712
	v_permlane32_swap_b32_e32 v70, v142
	s_waitcnt lgkmcnt(0)
	v_mfma_f32_16x16x32_bf16 v[58:61], v[62:65], v[34:37], v[58:61]
	ds_read_b128 v[62:65], v131 offset:47872
	v_permlane32_swap_b32_e32 v71, v143
	s_waitcnt lgkmcnt(0)
	v_mfma_f32_16x16x32_bf16 v[62:65], v[62:65], v[46:49], 0
	v_permlane32_swap_b32_e32 v72, v144
	v_permlane32_swap_b32_e32 v73, v145
	v_mfma_f32_16x16x32_bf16 v[62:65], v[66:69], v[42:45], v[62:65]
	ds_read_b128 v[66:69], v131 offset:48000
	v_permlane32_swap_b32_e32 v74, v146
	s_waitcnt lgkmcnt(0)
	v_mfma_f32_16x16x32_bf16 v[62:65], v[66:69], v[38:41], v[62:65]
	ds_read_b128 v[66:69], v131 offset:48064
	v_permlane32_swap_b32_e32 v75, v147
	s_waitcnt lgkmcnt(0)
	v_mfma_f32_16x16x32_bf16 v[62:65], v[66:69], v[34:37], v[62:65]
	ds_read_b128 v[66:69], v131 offset:52224
	v_permlane32_swap_b32_e32 v76, v148
	s_waitcnt lgkmcnt(0)
	v_mfma_f32_16x16x32_bf16 v[66:69], v[66:69], v[46:49], 0
	v_permlane32_swap_b32_e32 v77, v149
	v_permlane32_swap_b32_e32 v134, v150
	v_mfma_f32_16x16x32_bf16 v[66:69], v[158:161], v[42:45], v[66:69]
	ds_read_b128 v[158:161], v131 offset:52352
	v_permlane32_swap_b32_e32 v135, v151
	s_waitcnt lgkmcnt(0)
	v_mfma_f32_16x16x32_bf16 v[66:69], v[158:161], v[38:41], v[66:69]
	ds_read_b128 v[158:161], v131 offset:52416
	v_permlane32_swap_b32_e32 v136, v152
	s_waitcnt lgkmcnt(0)
	v_mfma_f32_16x16x32_bf16 v[66:69], v[158:161], v[34:37], v[66:69]
	ds_read_b128 v[158:161], v131 offset:56576
	v_permlane32_swap_b32_e32 v137, v153
	s_waitcnt lgkmcnt(0)
	v_mfma_f32_16x16x32_bf16 v[158:161], v[158:161], v[46:49], 0
	v_permlane32_swap_b32_e32 v138, v154
	v_permlane32_swap_b32_e32 v139, v155
	v_mfma_f32_16x16x32_bf16 v[158:161], v[162:165], v[42:45], v[158:161]
	ds_read_b128 v[162:165], v131 offset:56704
	v_permlane32_swap_b32_e32 v140, v156
	s_waitcnt lgkmcnt(0)
	v_mfma_f32_16x16x32_bf16 v[158:161], v[162:165], v[38:41], v[158:161]
	ds_read_b128 v[162:165], v131 offset:56768
	v_permlane32_swap_b32_e32 v141, v157
	s_waitcnt lgkmcnt(0)
	v_mfma_f32_16x16x32_bf16 v[158:161], v[162:165], v[34:37], v[158:161]
	ds_read_b128 v[162:165], v131 offset:60928
	s_waitcnt lgkmcnt(0)
	v_mfma_f32_16x16x32_bf16 v[162:165], v[162:165], v[46:49], 0
	v_mfma_f32_16x16x32_bf16 v[162:165], v[166:169], v[42:45], v[162:165]
	ds_read_b128 v[166:169], v131 offset:61056
	s_waitcnt lgkmcnt(0)
	v_mfma_f32_16x16x32_bf16 v[162:165], v[166:169], v[38:41], v[162:165]
	ds_read_b128 v[166:169], v131 offset:61120
	s_waitcnt lgkmcnt(0)
	v_mfma_f32_16x16x32_bf16 v[162:165], v[166:169], v[34:37], v[162:165]
	ds_read_b128 v[166:169], v131 offset:65280
	s_waitcnt lgkmcnt(0)
	v_mfma_f32_16x16x32_bf16 v[46:49], v[166:169], v[46:49], 0
	ds_read_b128 v[166:169], v131 offset:65344
	s_waitcnt lgkmcnt(0)
	v_mfma_f32_16x16x32_bf16 v[42:45], v[166:169], v[42:45], v[46:49]
	s_nop 4
	ds_read_b128 v[46:49], v131 offset:65408
	s_waitcnt lgkmcnt(0)
	v_mfma_f32_16x16x32_bf16 v[38:41], v[46:49], v[38:41], v[42:45]
	s_nop 2
	ds_read_b128 v[42:45], v131 offset:65472
	s_waitcnt lgkmcnt(0)
; __device__ __forceinline__ unsigned mono(float f) { const unsigned u = __float_as_uint(f); return (u & 0x80000000u) ? ~u : (u ^ 0x80000000u); }
; __device__ __forceinline__ void topk_phase(LAS unsigned char* lds, const bf16_t* qp, const bf16_t* keys, const float* SU, const float* SV, int* sel_e, float* sel_g, float* sel_su, int G, int b) {
;     ...
;             unsigned lo16[16];
; #pragma unroll
;             for (int mt = 0; mt < 4; ++mt)
; #pragma unroll
;                 for (int r = 0; r < 4; ++r) {
;                     T[p][mt * 4 + r] = (mono(acc[mt][r]) & ~127u) | (unsigned)(127 - (mt * 16 + fq * 4 + r));
;                     lo16[mt * 4 + r] = (mono(acc[mt + 4][r]) & ~127u) | (unsigned)(127 - ((mt + 4) * 16 + fq * 4 + r));
;                 }
;             SN_SORT16(T[p]); SN_SORT16(lo16);
	v_mfma_f32_16x16x32_bf16 v[34:37], v[42:45], v[34:37], v[38:41]
	s_nop 2
	v_ashrrev_i32_e32 v38, 31, v50
	v_bitop3_b32 v38, v50, v38, v132 bitop3:0x1e
	v_and_or_b32 v38, v38, s53, v98
	v_ashrrev_i32_e32 v39, 31, v66
	v_bitop3_b32 v39, v66, v39, v132 bitop3:0x1e
	v_and_or_b32 v39, v39, s53, v99
	v_ashrrev_i32_e32 v40, 31, v51
	v_bitop3_b32 v40, v51, v40, v132 bitop3:0x1e
	v_and_or_b32 v40, v40, s53, v100
	v_ashrrev_i32_e32 v41, 31, v67
	v_bitop3_b32 v41, v67, v41, v132 bitop3:0x1e
	v_and_or_b32 v41, v41, s53, v101
	v_ashrrev_i32_e32 v42, 31, v52
	v_bitop3_b32 v42, v52, v42, v132 bitop3:0x1e
	v_and_or_b32 v42, v42, s53, v102
	v_ashrrev_i32_e32 v43, 31, v68
	v_bitop3_b32 v43, v68, v43, v132 bitop3:0x1e
	v_and_or_b32 v43, v43, s53, v103
	v_ashrrev_i32_e32 v44, 31, v53
	v_bitop3_b32 v44, v53, v44, v132 bitop3:0x1e
	v_and_or_b32 v44, v44, s53, v104
	v_ashrrev_i32_e32 v45, 31, v69
	v_bitop3_b32 v45, v69, v45, v132 bitop3:0x1e
	v_and_or_b32 v45, v45, s53, v105
	v_ashrrev_i32_e32 v46, 31, v54
	v_bitop3_b32 v46, v54, v46, v132 bitop3:0x1e
	v_and_or_b32 v46, v46, s53, v106
	v_ashrrev_i32_e32 v47, 31, v158
	v_bitop3_b32 v47, v158, v47, v132 bitop3:0x1e
	v_and_or_b32 v47, v47, s53, v107
	v_ashrrev_i32_e32 v48, 31, v55
	v_bitop3_b32 v48, v55, v48, v132 bitop3:0x1e
	v_and_or_b32 v48, v48, s53, v108
	v_ashrrev_i32_e32 v49, 31, v159
	v_bitop3_b32 v49, v159, v49, v132 bitop3:0x1e
	v_and_or_b32 v49, v49, s53, v109
	v_ashrrev_i32_e32 v50, 31, v56
	v_bitop3_b32 v50, v56, v50, v132 bitop3:0x1e
	v_and_or_b32 v50, v50, s53, v110
	v_ashrrev_i32_e32 v51, 31, v160
	v_bitop3_b32 v51, v160, v51, v132 bitop3:0x1e
	v_max_u32_e32 v160, v39, v41
	v_ashrrev_i32_e32 v52, 31, v57
	v_bitop3_b32 v52, v57, v52, v132 bitop3:0x1e
	v_min_u32_e32 v39, v39, v41
	v_ashrrev_i32_e32 v53, 31, v161
	v_bitop3_b32 v53, v161, v53, v132 bitop3:0x1e
	v_max_u32_e32 v41, v43, v45
	v_ashrrev_i32_e32 v54, 31, v58
	v_cmp_lt_i32_e32 vcc, -1, v162
	v_bitop3_b32 v54, v58, v54, v132 bitop3:0x1e
	v_min_u32_e32 v43, v43, v45
	v_cndmask_b32_e32 v55, -1, v132, vcc
	v_and_or_b32 v51, v51, s53, v111
	v_and_or_b32 v52, v52, s53, v112
	v_ashrrev_i32_e32 v56, 31, v59
	v_cmp_lt_i32_e32 vcc, -1, v163
	v_bitop3_b32 v56, v59, v56, v132 bitop3:0x1e
	v_and_or_b32 v53, v53, s53, v113
	v_cndmask_b32_e32 v57, -1, v132, vcc
	v_max_u32_e32 v45, v160, v41
	v_min_u32_e32 v41, v160, v41
	v_ashrrev_i32_e32 v58, 31, v60
	v_cmp_lt_i32_e32 vcc, -1, v164
	v_bitop3_b32 v58, v60, v58, v132 bitop3:0x1e
	v_max_u32_e32 v160, v39, v43
	v_cndmask_b32_e32 v59, -1, v132, vcc
	v_min_u32_e32 v39, v39, v43
	v_max_u32_e32 v43, v160, v41
	v_ashrrev_i32_e32 v60, 31, v61
	v_cmp_lt_i32_e32 vcc, -1, v165
	v_bitop3_b32 v60, v61, v60, v132 bitop3:0x1e
	v_min_u32_e32 v41, v160, v41
	v_cndmask_b32_e32 v61, -1, v132, vcc
	v_max_u32_e32 v160, v47, v49
	v_min_u32_e32 v47, v47, v49
	v_ashrrev_i32_e32 v66, 31, v62
	v_bitop3_b32 v62, v62, v66, v132 bitop3:0x1e
	v_max_u32_e32 v49, v51, v53
	v_ashrrev_i32_e32 v66, 31, v34
	v_bitop3_b32 v34, v34, v66, v132 bitop3:0x1e
	v_min_u32_e32 v51, v51, v53
	v_ashrrev_i32_e32 v66, 31, v63
	v_bitop3_b32 v63, v63, v66, v132 bitop3:0x1e
	v_max_u32_e32 v53, v160, v49
	v_ashrrev_i32_e32 v66, 31, v35
	v_bitop3_b32 v35, v35, v66, v132 bitop3:0x1e
	v_min_u32_e32 v49, v160, v49
	v_ashrrev_i32_e32 v66, 31, v64
	v_bitop3_b32 v64, v64, v66, v132 bitop3:0x1e
	v_max_u32_e32 v160, v47, v51
	v_ashrrev_i32_e32 v66, 31, v36
	v_bitop3_b32 v36, v36, v66, v132 bitop3:0x1e
	v_min_u32_e32 v47, v47, v51
	v_ashrrev_i32_e32 v66, 31, v65
	v_cmp_lt_i32_e32 vcc, -1, v37
	v_bitop3_b32 v65, v65, v66, v132 bitop3:0x1e
	v_max_u32_e32 v51, v160, v49
	v_cndmask_b32_e32 v66, -1, v132, vcc
	v_xor_b32_e32 v37, v66, v37
	v_max_u32_e32 v66, v38, v40
	v_min_u32_e32 v38, v38, v40
	v_max_u32_e32 v40, v42, v44
	v_min_u32_e32 v42, v42, v44
	v_max_u32_e32 v44, v66, v40
	v_min_u32_e32 v40, v66, v40
	v_max_u32_e32 v66, v38, v42
	v_min_u32_e32 v38, v38, v42
	v_max_u32_e32 v42, v66, v40
	v_min_u32_e32 v40, v66, v40
	v_max_u32_e32 v66, v46, v48
	v_min_u32_e32 v46, v46, v48
	v_max_u32_e32 v48, v50, v52
	v_min_u32_e32 v50, v50, v52
	v_max_u32_e32 v52, v66, v48
	v_min_u32_e32 v48, v66, v48
	v_max_u32_e32 v66, v46, v50
	v_min_u32_e32 v46, v46, v50
	v_max_u32_e32 v50, v66, v48
	v_min_u32_e32 v48, v66, v48
	v_min_u32_e32 v49, v160, v49
	v_max_u32_e32 v66, v44, v52
	v_min_u32_e32 v44, v44, v52
	v_max_u32_e32 v52, v40, v48
	v_max_u32_e32 v160, v45, v53
	v_min_u32_e32 v45, v45, v53
	v_max_u32_e32 v53, v41, v49
	v_xor_b32_e32 v55, v55, v162
	v_xor_b32_e32 v57, v57, v163
	v_xor_b32_e32 v59, v59, v164
	v_xor_b32_e32 v61, v61, v165
	v_min_u32_e32 v40, v40, v48
	v_max_u32_e32 v48, v52, v44
	v_min_u32_e32 v44, v52, v44
	v_max_u32_e32 v52, v42, v50
	v_min_u32_e32 v42, v42, v50
	v_max_u32_e32 v50, v38, v46
	v_min_u32_e32 v41, v41, v49
	v_max_u32_e32 v49, v53, v45
	v_min_u32_e32 v45, v53, v45
	v_max_u32_e32 v53, v43, v51
	v_min_u32_e32 v43, v43, v51
	v_max_u32_e32 v51, v39, v47
	v_and_or_b32 v54, v54, s53, v114
	v_and_or_b32 v55, v55, s53, v115
	v_and_or_b32 v56, v56, s53, v116
	v_and_or_b32 v57, v57, s53, v117
	v_and_or_b32 v58, v58, s53, v118
	v_and_or_b32 v59, v59, s53, v119
	v_and_or_b32 v60, v60, s53, v120
	v_and_or_b32 v61, v61, s53, v121
	v_min_u32_e32 v38, v38, v46
	v_max_u32_e32 v46, v50, v42
	v_min_u32_e32 v42, v50, v42
	v_min_u32_e32 v39, v39, v47
	v_max_u32_e32 v47, v51, v43
	v_min_u32_e32 v43, v51, v43
	v_max_u32_e32 v50, v52, v48
	v_min_u32_e32 v48, v52, v48
	v_max_u32_e32 v52, v46, v44
	v_min_u32_e32 v44, v46, v44
	v_max_u32_e32 v46, v42, v40
	v_min_u32_e32 v40, v42, v40
	v_max_u32_e32 v42, v54, v56
	v_min_u32_e32 v54, v54, v56
	v_max_u32_e32 v56, v58, v60
; __device__ __forceinline__ unsigned mono(float f) { const unsigned u = __float_as_uint(f); return (u & 0x80000000u) ? ~u : (u ^ 0x80000000u); }
; __device__ __forceinline__ void topk_phase(LAS unsigned char* lds, const bf16_t* qp, const bf16_t* keys, const float* SU, const float* SV, int* sel_e, float* sel_g, float* sel_su, int G, int b) {
;     ...
;             unsigned lo16[16];
; #pragma unroll
;             for (int mt = 0; mt < 4; ++mt)
; #pragma unroll
;                 for (int r = 0; r < 4; ++r) {
;                     T[p][mt * 4 + r] = (mono(acc[mt][r]) & ~127u) | (unsigned)(127 - (mt * 16 + fq * 4 + r));
;                     lo16[mt * 4 + r] = (mono(acc[mt + 4][r]) & ~127u) | (unsigned)(127 - ((mt + 4) * 16 + fq * 4 + r));
;                 }
;             SN_SORT16(T[p]); SN_SORT16(lo16);
; #pragma unroll
;             for (int i = 0; i < 16; ++i) T[p][i] = umax_(T[p][i], lo16[15 - i]);
;             SN_BITONIC16(T[p]);
	v_min_u32_e32 v58, v58, v60
	v_max_u32_e32 v51, v53, v49
	v_min_u32_e32 v49, v53, v49
	v_max_u32_e32 v53, v47, v45
	v_min_u32_e32 v45, v47, v45
	v_max_u32_e32 v47, v43, v41
	v_min_u32_e32 v41, v43, v41
	v_max_u32_e32 v43, v55, v57
	v_min_u32_e32 v55, v55, v57
	v_max_u32_e32 v57, v59, v61
	v_min_u32_e32 v59, v59, v61
	v_and_or_b32 v62, v62, s53, v122
	v_and_or_b32 v34, v34, s53, v123
	v_and_or_b32 v63, v63, s53, v124
	v_and_or_b32 v35, v35, s53, v125
	v_and_or_b32 v64, v64, s53, v126
	v_and_or_b32 v36, v36, s53, v127
	v_and_or_b32 v65, v65, s53, v128
	v_and_or_b32 v37, v37, s53, v129
	v_max_u32_e32 v60, v42, v56
	v_min_u32_e32 v42, v42, v56
	v_max_u32_e32 v56, v54, v58
	v_max_u32_e32 v61, v43, v57
	v_min_u32_e32 v43, v43, v57
	v_max_u32_e32 v57, v55, v59
	v_min_u32_e32 v54, v54, v58
	v_max_u32_e32 v58, v56, v42
	v_min_u32_e32 v42, v56, v42
	v_max_u32_e32 v56, v62, v63
	v_min_u32_e32 v62, v62, v63
	v_max_u32_e32 v63, v64, v65
	v_min_u32_e32 v64, v64, v65
	v_min_u32_e32 v55, v55, v59
	v_max_u32_e32 v59, v57, v43
	v_min_u32_e32 v43, v57, v43
	v_max_u32_e32 v57, v34, v35
	v_min_u32_e32 v34, v34, v35
	v_max_u32_e32 v35, v36, v37
	v_min_u32_e32 v36, v36, v37
	v_max_u32_e32 v65, v56, v63
	v_min_u32_e32 v56, v56, v63
	v_max_u32_e32 v63, v62, v64
	v_max_u32_e32 v37, v57, v35
	v_min_u32_e32 v35, v57, v35
	v_max_u32_e32 v57, v34, v36
	v_min_u32_e32 v62, v62, v64
	v_max_u32_e32 v64, v63, v56
	v_min_u32_e32 v56, v63, v56
	v_min_u32_e32 v34, v34, v36
	v_max_u32_e32 v36, v57, v35
	v_min_u32_e32 v35, v57, v35
	v_max_u32_e32 v63, v60, v65
	v_min_u32_e32 v60, v60, v65
	v_max_u32_e32 v65, v42, v56
	v_max_u32_e32 v57, v61, v37
	v_min_u32_e32 v37, v61, v37
	v_max_u32_e32 v61, v43, v35
	v_min_u32_e32 v42, v42, v56
	v_max_u32_e32 v56, v65, v60
	v_min_u32_e32 v60, v65, v60
	v_max_u32_e32 v65, v58, v64
	v_min_u32_e32 v58, v58, v64
	v_max_u32_e32 v64, v54, v62
	v_min_u32_e32 v35, v43, v35
	v_max_u32_e32 v43, v61, v37
	v_min_u32_e32 v37, v61, v37
	v_max_u32_e32 v61, v59, v36
	v_min_u32_e32 v36, v59, v36
	v_max_u32_e32 v59, v55, v34
	v_min_u32_e32 v54, v54, v62
	v_max_u32_e32 v62, v64, v58
	v_min_u32_e32 v34, v55, v34
	v_max_u32_e32 v55, v59, v36
	v_min_u32_e32 v58, v64, v58
	v_max_u32_e32 v64, v65, v56
	v_min_u32_e32 v56, v65, v56
	v_max_u32_e32 v65, v62, v60
	v_min_u32_e32 v60, v62, v60
	v_min_u32_e32 v36, v59, v36
	v_max_u32_e32 v59, v61, v43
	v_min_u32_e32 v43, v61, v43
	v_max_u32_e32 v61, v55, v37
	v_min_u32_e32 v37, v55, v37
	v_max_u32_e32 v62, v58, v42
	v_min_u32_e32 v42, v58, v42
	v_min_u32_e32 v58, v66, v63
	v_max_u32_e32 v67, v44, v60
	v_max_u32_e32 v55, v36, v35
	v_min_u32_e32 v35, v36, v35
	v_min_u32_e32 v36, v160, v57
	v_max_u32_e32 v161, v45, v37
	v_min_u32_e32 v44, v44, v60
	v_max_u32_e32 v60, v67, v58
	v_min_u32_e32 v58, v67, v58
	v_max_u32_e32 v67, v48, v56
	v_min_u32_e32 v48, v48, v56
	v_max_u32_e32 v56, v40, v42
	v_min_u32_e32 v37, v45, v37
	v_max_u32_e32 v45, v161, v36
	v_min_u32_e32 v36, v161, v36
	v_max_u32_e32 v161, v49, v43
	v_min_u32_e32 v43, v49, v43
	v_max_u32_e32 v49, v41, v35
	v_min_u32_e32 v40, v40, v42
	v_max_u32_e32 v42, v56, v48
	v_min_u32_e32 v48, v56, v48
	v_min_u32_e32 v35, v41, v35
	v_max_u32_e32 v41, v49, v43
	v_min_u32_e32 v43, v49, v43
	v_max_u32_e32 v56, v67, v60
	v_min_u32_e32 v60, v67, v60
	v_max_u32_e32 v67, v42, v58
	v_min_u32_e32 v42, v42, v58
	v_max_u32_e32 v58, v48, v44
	v_min_u32_e32 v44, v48, v44
	v_max_u32_e32 v48, v50, v64
	v_min_u32_e32 v50, v50, v64
	v_max_u32_e32 v64, v46, v62
	v_max_u32_e32 v49, v161, v45
	v_min_u32_e32 v45, v161, v45
	v_max_u32_e32 v161, v41, v36
	v_min_u32_e32 v36, v41, v36
	v_max_u32_e32 v41, v43, v37
	v_min_u32_e32 v37, v43, v37
	v_max_u32_e32 v43, v51, v59
	v_min_u32_e32 v51, v51, v59
	v_max_u32_e32 v59, v47, v55
	v_min_u32_e32 v46, v46, v62
	v_max_u32_e32 v62, v64, v50
	v_min_u32_e32 v50, v64, v50
	v_max_u32_e32 v64, v52, v65
	v_min_u32_e32 v52, v52, v65
	v_max_u32_e32 v65, v38, v54
	v_min_u32_e32 v47, v47, v55
	v_max_u32_e32 v55, v59, v51
	v_min_u32_e32 v51, v59, v51
	v_max_u32_e32 v59, v53, v61
	v_min_u32_e32 v53, v53, v61
	v_max_u32_e32 v61, v39, v34
	v_min_u32_e32 v38, v38, v54
	v_max_u32_e32 v54, v65, v52
	v_min_u32_e32 v52, v65, v52
	v_min_u32_e32 v34, v39, v34
	v_max_u32_e32 v39, v61, v53
	v_min_u32_e32 v53, v61, v53
	v_max_u32_e32 v65, v64, v62
	v_min_u32_e32 v62, v64, v62
	v_max_u32_e32 v64, v54, v50
	v_min_u32_e32 v50, v54, v50
	v_max_u32_e32 v54, v52, v46
	v_min_u32_e32 v46, v52, v46
	v_max_u32_e32 v61, v59, v55
	v_min_u32_e32 v55, v59, v55
	v_max_u32_e32 v59, v39, v51
	v_min_u32_e32 v39, v39, v51
	v_max_u32_e32 v51, v53, v47
	v_min_u32_e32 v47, v53, v47
	v_min_u32_e32 v52, v48, v56
	v_min_u32_e32 v68, v65, v60
	v_min_u32_e32 v69, v62, v67
	v_min_u32_e32 v96, v64, v42
	v_min_u32_e32 v97, v50, v58
	v_min_u32_e32 v158, v54, v44
	v_min_u32_e32 v159, v46, v40
	v_min_u32_e32 v53, v43, v49
	v_min_u32_e32 v162, v61, v45
	v_min_u32_e32 v163, v55, v161
	v_min_u32_e32 v164, v59, v36
	v_min_u32_e32 v165, v39, v41
	v_min_u32_e32 v166, v51, v37
	v_min_u32_e32 v167, v47, v35
	v_max3_u32 v34, v66, v63, v34
	v_max3_u32 v48, v48, v56, v167
	v_max3_u32 v35, v52, v47, v35
	v_max3_u32 v47, v65, v60, v166
	v_max3_u32 v37, v68, v51, v37
	v_max3_u32 v51, v62, v67, v165
	v_max3_u32 v39, v69, v39, v41
	v_max3_u32 v41, v64, v42, v164
	v_max3_u32 v36, v96, v59, v36
	v_max3_u32 v42, v50, v58, v163
	v_max3_u32 v50, v97, v55, v161
	v_max3_u32 v44, v54, v44, v162
	v_max3_u32 v45, v158, v61, v45
	v_max3_u32 v40, v46, v40, v53
	v_max3_u32 v43, v159, v43, v49
	v_max3_u32 v38, v38, v160, v57
	v_max_u32_e32 v46, v34, v36
	v_min_u32_e32 v34, v34, v36
	v_max_u32_e32 v36, v48, v42
	v_min_u32_e32 v42, v48, v42
; __device__ __forceinline__ void topk_phase(LAS unsigned char* lds, const bf16_t* qp, const bf16_t* keys, const float* SU, const float* SV, int* sel_e, float* sel_g, float* sel_su, int G, int b) {
;     ...
;             SN_SORT16(T[p]); SN_SORT16(lo16);
; #pragma unroll
;             for (int i = 0; i < 16; ++i) T[p][i] = umax_(T[p][i], lo16[15 - i]);
;             SN_BITONIC16(T[p]);
;             TOPK_XMERGE(T[p], 16); TOPK_XMERGE(T[p], 32);
	v_max_u32_e32 v48, v35, v50
	v_min_u32_e32 v35, v35, v50
	v_max_u32_e32 v49, v47, v44
	v_min_u32_e32 v44, v47, v44
	v_max_u32_e32 v47, v37, v45
	v_min_u32_e32 v37, v37, v45
	v_max_u32_e32 v45, v51, v40
	v_min_u32_e32 v40, v51, v40
	v_max_u32_e32 v50, v39, v43
	v_min_u32_e32 v39, v39, v43
	v_max_u32_e32 v43, v41, v38
	v_min_u32_e32 v38, v41, v38
	v_max_u32_e32 v41, v46, v47
	v_min_u32_e32 v46, v46, v47
	v_max_u32_e32 v47, v36, v45
	v_min_u32_e32 v36, v36, v45
	v_max_u32_e32 v45, v48, v50
	v_min_u32_e32 v48, v48, v50
	v_max_u32_e32 v50, v49, v43
	v_min_u32_e32 v43, v49, v43
	v_max_u32_e32 v49, v34, v37
	v_min_u32_e32 v34, v34, v37
	v_max_u32_e32 v37, v42, v40
	v_min_u32_e32 v40, v42, v40
	v_max_u32_e32 v42, v35, v39
	v_min_u32_e32 v35, v35, v39
	v_max_u32_e32 v39, v44, v38
	v_min_u32_e32 v38, v44, v38
	v_max_u32_e32 v44, v41, v45
	v_min_u32_e32 v41, v41, v45
	v_max_u32_e32 v45, v47, v50
	v_min_u32_e32 v47, v47, v50
	v_max_u32_e32 v50, v46, v48
	v_min_u32_e32 v46, v46, v48
	v_max_u32_e32 v48, v36, v43
	v_min_u32_e32 v36, v36, v43
	v_max_u32_e32 v43, v49, v42
	v_min_u32_e32 v42, v49, v42
	v_max_u32_e32 v49, v37, v39
	v_min_u32_e32 v37, v37, v39
	v_max_u32_e32 v39, v34, v35
	v_min_u32_e32 v34, v34, v35
	v_max_u32_e32 v35, v40, v38
	v_min_u32_e32 v38, v40, v38
	v_max_u32_e32 v40, v44, v45
	v_min_u32_e32 v44, v44, v45
	v_max_u32_e32 v45, v41, v47
	v_min_u32_e32 v41, v41, v47
	v_max_u32_e32 v47, v50, v48
	v_min_u32_e32 v48, v50, v48
	v_max_u32_e32 v50, v46, v36
	v_min_u32_e32 v36, v46, v36
	v_max_u32_e32 v46, v43, v49
	v_min_u32_e32 v43, v43, v49
	v_max_u32_e32 v49, v42, v37
	v_min_u32_e32 v37, v42, v37
	v_max_u32_e32 v42, v39, v35
	v_min_u32_e32 v35, v39, v35
	v_max_u32_e32 v39, v34, v38
	v_min_u32_e32 v34, v34, v38
	v_mov_b32_e32 v38, v40
	v_mov_b32_e32 v51, v44
	v_mov_b32_e32 v52, v45
	v_mov_b32_e32 v53, v41
	v_mov_b32_e32 v54, v47
	v_mov_b32_e32 v55, v48
	v_mov_b32_e32 v56, v50
	v_mov_b32_e32 v57, v36
	v_mov_b32_e32 v58, v46
	v_mov_b32_e32 v59, v43
	v_mov_b32_e32 v60, v49
	v_mov_b32_e32 v61, v37
	v_mov_b32_e32 v62, v42
	v_mov_b32_e32 v63, v35
	v_mov_b32_e32 v64, v39
	v_mov_b32_e32 v65, v34
	v_permlane16_swap_b32_e32 v40, v38
	v_permlane16_swap_b32_e32 v44, v51
	v_permlane16_swap_b32_e32 v45, v52
	v_permlane16_swap_b32_e32 v41, v53
	v_permlane16_swap_b32_e32 v47, v54
	v_permlane16_swap_b32_e32 v48, v55
	v_permlane16_swap_b32_e32 v50, v56
	v_permlane16_swap_b32_e32 v36, v57
	v_permlane16_swap_b32_e32 v46, v58
	v_permlane16_swap_b32_e32 v43, v59
	v_permlane16_swap_b32_e32 v49, v60
	v_permlane16_swap_b32_e32 v37, v61
	v_permlane16_swap_b32_e32 v42, v62
	v_permlane16_swap_b32_e32 v35, v63
	v_permlane16_swap_b32_e32 v39, v64
	v_permlane16_swap_b32_e32 v34, v65
	v_max_u32_e32 v40, v40, v65
	v_max_u32_e32 v44, v44, v64
	v_max_u32_e32 v45, v45, v63
	v_max_u32_e32 v41, v41, v62
	v_max_u32_e32 v47, v47, v61
	v_max_u32_e32 v48, v48, v60
	v_max_u32_e32 v50, v50, v59
	v_max_u32_e32 v36, v36, v58
	v_max_u32_e32 v46, v46, v57
	v_max_u32_e32 v43, v43, v56
	v_max_u32_e32 v49, v49, v55
	v_max_u32_e32 v37, v37, v54
	v_max_u32_e32 v42, v42, v53
	v_max_u32_e32 v35, v35, v52
	v_max_u32_e32 v39, v39, v51
	v_max_u32_e32 v34, v34, v38
	v_max_u32_e32 v38, v40, v46
	v_min_u32_e32 v40, v40, v46
	v_max_u32_e32 v46, v44, v43
	v_min_u32_e32 v43, v44, v43
	v_max_u32_e32 v44, v45, v49
	v_min_u32_e32 v45, v45, v49
	v_max_u32_e32 v49, v41, v37
	v_min_u32_e32 v37, v41, v37
	v_max_u32_e32 v41, v47, v42
	v_min_u32_e32 v42, v47, v42
	v_max_u32_e32 v47, v48, v35
	v_min_u32_e32 v35, v48, v35
	v_max_u32_e32 v48, v50, v39
	v_min_u32_e32 v39, v50, v39
	v_max_u32_e32 v50, v36, v34
	v_min_u32_e32 v34, v36, v34
	v_max_u32_e32 v36, v38, v41
	v_min_u32_e32 v38, v38, v41
	v_max_u32_e32 v41, v46, v47
	v_min_u32_e32 v46, v46, v47
	v_max_u32_e32 v47, v44, v48
	v_min_u32_e32 v44, v44, v48
	v_max_u32_e32 v48, v49, v50
	v_min_u32_e32 v49, v49, v50
	v_max_u32_e32 v50, v40, v42
	v_min_u32_e32 v40, v40, v42
	v_max_u32_e32 v42, v43, v35
	v_min_u32_e32 v35, v43, v35
	v_max_u32_e32 v43, v45, v39
	v_min_u32_e32 v39, v45, v39
	v_max_u32_e32 v45, v37, v34
	v_min_u32_e32 v34, v37, v34
	v_max_u32_e32 v37, v36, v47
	v_min_u32_e32 v47, v36, v47
	v_max_u32_e32 v51, v41, v48
	v_min_u32_e32 v41, v41, v48
	v_max_u32_e32 v48, v38, v44
	v_min_u32_e32 v44, v38, v44
	v_max_u32_e32 v52, v46, v49
	v_min_u32_e32 v46, v46, v49
	v_max_u32_e32 v49, v50, v43
	v_min_u32_e32 v50, v50, v43
	v_max_u32_e32 v53, v42, v45
	v_min_u32_e32 v55, v42, v45
	v_max_u32_e32 v58, v40, v39
	v_min_u32_e32 v59, v40, v39
	v_max_u32_e32 v60, v35, v34
	v_min_u32_e32 v34, v35, v34
	v_max_u32_e32 v36, v37, v51
	v_min_u32_e32 v37, v37, v51
; __device__ __forceinline__ unsigned mono(float f) { const unsigned u = __float_as_uint(f); return (u & 0x80000000u) ? ~u : (u ^ 0x80000000u); }
; __device__ __forceinline__ float unmono(unsigned u) { return __uint_as_float((u & 0x80000000u) ? (u ^ 0x80000000u) : ~u); }
; __device__ __forceinline__ void topk_phase(LAS unsigned char* lds, const bf16_t* qp, const bf16_t* keys, const float* SU, const float* SV, int* sel_e, float* sel_g, float* sel_su, int G, int b) {
;     ...
;             TOPK_XMERGE(T[p], 16); TOPK_XMERGE(T[p], 32);
;         }
;         float v1[16], v2[16];
; #pragma unroll
;         for (int i = 0; i < 16; ++i) { v1[i] = unmono(T[0][i] & ~127u); v2[i] = unmono(T[1][i] & ~127u); }
;         unsigned ck[16];
; #pragma unroll
;         for (int sidx = 0; sidx < 13; ++sidx) {
;             unsigned keyk[4];
; #pragma unroll
;             for (int k = 0; k < 4; ++k) {
;                 const int c = 4 * sidx + k;
;                 if (c < 50) { const int ci = cand_i(c), cj = cand_j(c); keyk[k] = (mono(v1[ci] + v2[cj]) & ~255u) | (unsigned)(255 - (ci * 16 + cj)); }
;                 else keyk[k] = 0u;
;             }
;             ck[sidx] = fq == 0 ? keyk[0] : fq == 1 ? keyk[1] : fq == 2 ? keyk[2] : keyk[3];
;         }
	v_max_u32_e32 v38, v47, v41
	v_min_u32_e32 v39, v47, v41
	v_max_u32_e32 v40, v48, v52
	v_min_u32_e32 v41, v48, v52
	v_max_u32_e32 v42, v44, v46
	v_min_u32_e32 v43, v44, v46
	v_max_u32_e32 v44, v49, v53
	v_min_u32_e32 v45, v49, v53
	v_max_u32_e32 v54, v50, v55
	v_min_u32_e32 v56, v50, v55
	v_max_u32_e32 v57, v58, v60
	v_min_u32_e32 v66, v58, v60
	v_max_u32_e32 v67, v59, v34
	v_min_u32_e32 v68, v59, v34
	v_mov_b32_e32 v69, v36
	v_mov_b32_e32 v158, v37
	v_mov_b32_e32 v159, v38
	v_mov_b32_e32 v160, v39
	v_mov_b32_e32 v161, v40
	v_mov_b32_e32 v162, v41
	v_mov_b32_e32 v163, v42
	v_mov_b32_e32 v97, v43
	v_mov_b32_e32 v53, v44
	v_mov_b32_e32 v52, v45
	v_mov_b32_e32 v51, v54
	v_mov_b32_e32 v50, v56
	v_mov_b32_e32 v49, v57
	v_mov_b32_e32 v48, v66
	v_mov_b32_e32 v47, v67
	v_mov_b32_e32 v46, v68
	v_permlane32_swap_b32_e32 v36, v69
	v_permlane32_swap_b32_e32 v37, v158
	v_permlane32_swap_b32_e32 v38, v159
	v_permlane32_swap_b32_e32 v39, v160
	v_permlane32_swap_b32_e32 v40, v161
	v_permlane32_swap_b32_e32 v41, v162
	v_permlane32_swap_b32_e32 v42, v163
	v_permlane32_swap_b32_e32 v43, v97
	v_permlane32_swap_b32_e32 v44, v53
	v_permlane32_swap_b32_e32 v45, v52
	v_permlane32_swap_b32_e32 v54, v51
	v_permlane32_swap_b32_e32 v56, v50
	v_permlane32_swap_b32_e32 v57, v49
	v_permlane32_swap_b32_e32 v66, v48
	v_permlane32_swap_b32_e32 v67, v47
	v_permlane32_swap_b32_e32 v68, v46
	v_max_u32_e32 v59, v70, v157
	v_max_u32_e32 v60, v71, v156
	v_max_u32_e32 v61, v72, v155
	v_max_u32_e32 v62, v73, v154
	v_max_u32_e32 v63, v74, v153
	v_max_u32_e32 v64, v75, v152
	v_max_u32_e32 v65, v76, v151
	v_max_u32_e32 v70, v77, v150
	v_max_u32_e32 v71, v134, v149
	v_max_u32_e32 v72, v135, v148
	v_max_u32_e32 v73, v136, v147
	v_max_u32_e32 v74, v137, v146
	v_max_u32_e32 v75, v138, v145
	v_max_u32_e32 v76, v139, v144
	v_max_u32_e32 v77, v140, v143
	v_max_u32_e32 v96, v141, v142
	v_max_u32_e32 v55, v59, v71
	v_max_u32_e32 v135, v60, v72
	v_max_u32_e32 v136, v61, v73
	v_max_u32_e32 v137, v62, v74
	v_max_u32_e32 v138, v63, v75
	v_max_u32_e32 v139, v64, v76
	v_max_u32_e32 v140, v65, v77
	v_max_u32_e32 v141, v70, v96
	v_max_u32_e32 v46, v36, v46
	v_max_u32_e32 v47, v37, v47
	v_max_u32_e32 v48, v38, v48
	v_max_u32_e32 v49, v39, v49
	v_max_u32_e32 v50, v40, v50
	v_max_u32_e32 v51, v41, v51
	v_max_u32_e32 v52, v42, v52
	v_max_u32_e32 v53, v43, v53
	v_max_u32_e32 v97, v44, v97
	v_max_u32_e32 v134, v45, v163
	v_max_u32_e32 v143, v54, v162
	v_max_u32_e32 v149, v56, v161
	v_max_u32_e32 v150, v57, v160
	v_max_u32_e32 v151, v66, v159
	v_max_u32_e32 v152, v67, v158
	v_max_u32_e32 v153, v68, v69
	v_max_u32_e32 v58, v55, v138
	v_max_u32_e32 v144, v135, v139
	v_max_u32_e32 v145, v136, v140
	v_max_u32_e32 v146, v137, v141
	v_max_u32_e32 v36, v46, v97
	v_max_u32_e32 v37, v47, v134
	v_max_u32_e32 v42, v48, v143
	v_max_u32_e32 v43, v49, v149
	v_max_u32_e32 v44, v50, v150
	v_max_u32_e32 v45, v51, v151
	v_max_u32_e32 v69, v52, v152
	v_max_u32_e32 v147, v53, v153
	v_max_u32_e32 v35, v58, v145
	v_max_u32_e32 v142, v144, v146
	v_max_u32_e32 v38, v36, v44
	v_max_u32_e32 v39, v37, v45
	v_max_u32_e32 v40, v42, v69
	v_max_u32_e32 v41, v43, v147
	v_max_u32_e32 v34, v35, v142
	v_max_u32_e32 v54, v38, v40
	v_min_u32_e32 v56, v38, v40
	v_max_u32_e32 v40, v39, v41
	v_min_u32_e32 v41, v39, v41
	v_min_u32_e32 v39, v54, v40
	v_cmp_lt_i32_e32 vcc, -1, v34
	v_max_u32_e32 v38, v54, v40
	v_max_u32_e32 v40, v56, v41
	v_cndmask_b32_e64 v54, v132, -1, vcc
	v_min_u32_e32 v41, v56, v41
	v_ashrrev_i32_e32 v66, 31, v39
	v_bitop3_b32 v67, v39, v66, s12 bitop3:0x93
	v_ashrrev_i32_e32 v68, 31, v38
	v_bitop3_b32 v66, v38, v68, s12 bitop3:0x93
	v_bitop3_b32 v54, v54, v34, s53 bitop3:0x78
	v_ashrrev_i32_e32 v57, 31, v41
	v_ashrrev_i32_e32 v148, 31, v40
	v_bitop3_b32 v57, v41, v57, s12 bitop3:0x93
	v_bitop3_b32 v56, v40, v148, s12 bitop3:0x93
	v_add_f32_e32 v68, v66, v54
	v_cmp_lt_i32_e32 vcc, -1, v68
	s_nop 1
	v_cndmask_b32_e32 v148, -1, v132, vcc
	v_bitop3_b32 v68, v148, s0, v68 bitop3:0xde
	v_cmp_lt_i32_e32 vcc, 0, v1
	s_and_saveexec_b64 s[0:1], vcc
	s_cbranch_execz .LBB0_665
	v_cmp_ne_u32_e32 vcc, 1, v1
	s_and_saveexec_b64 s[4:5], vcc
	s_xor_b64 s[4:5], exec, s[4:5]
	s_cbranch_execz .LBB0_662
	v_pk_add_f32 v[154:155], v[54:55], v[56:57] op_sel_hi:[0,1]
	v_cmp_lt_i32_e32 vcc, -1, v155
	v_and_b32_e32 v148, 0xffffff00, v155
	s_movk_i32 s6, 0xfc
	v_cndmask_b32_e32 v68, v133, v132, vcc
	v_cmp_lt_i32_e32 vcc, -1, v154
	v_bitop3_b32 v68, v68, s6, v148 bitop3:0xde
	v_and_b32_e32 v154, 0xffffff00, v154
	v_cndmask_b32_e32 v148, v133, v132, vcc
	s_movk_i32 s6, 0xfd
	v_bitop3_b32 v148, v148, s6, v154 bitop3:0xde
	v_cndmask_b32_e64 v68, v68, v148, s[38:39]

; __device__ __forceinline__ unsigned mono(float f) { const unsigned u = __float_as_uint(f); return (u & 0x80000000u) ? ~u : (u ^ 0x80000000u); }
; __device__ __forceinline__ float unmono(unsigned u) { return __uint_as_float((u & 0x80000000u) ? (u ^ 0x80000000u) : ~u); }
; __device__ __forceinline__ void topk_phase(LAS unsigned char* lds, const bf16_t* qp, const bf16_t* keys, const float* SU, const float* SV, int* sel_e, float* sel_g, float* sel_su, int G, int b) {
;     ...
;         for (int i = 0; i < 16; ++i) { v1[i] = unmono(T[0][i] & ~127u); v2[i] = unmono(T[1][i] & ~127u); }
;         unsigned ck[16];
; #pragma unroll
;         for (int sidx = 0; sidx < 13; ++sidx) {
;             unsigned keyk[4];
; #pragma unroll
;             for (int k = 0; k < 4; ++k) {
;                 const int c = 4 * sidx + k;
;                 if (c < 50) { const int ci = cand_i(c), cj = cand_j(c); keyk[k] = (mono(v1[ci] + v2[cj]) & ~255u) | (unsigned)(255 - (ci * 16 + cj)); }
;                 else keyk[k] = 0u;
;             }
;             ck[sidx] = fq == 0 ? keyk[0] : fq == 1 ? keyk[1] : fq == 2 ? keyk[2] : keyk[3];
;         }
.LBB0_669:
	s_or_saveexec_b64 s[0:1], s[4:5]
	v_cndmask_b32_e64 v147, v132, -1, vcc
	v_bitop3_b32 v147, v147, v42, s53 bitop3:0x78
	s_xor_b64 exec, exec, s[0:1]
	v_add_f32_e32 v69, v54, v147
	v_cmp_lt_i32_e32 vcc, -1, v69
	s_nop 1
	v_cndmask_b32_e32 v154, -1, v132, vcc
	v_bitop3_b32 v69, v154, s60, v69 bitop3:0x48
	v_or_b32_e32 v69, 0xfb, v69
	s_or_b64 exec, exec, s[0:1]
	v_min_u32_e32 v154, v46, v97
	v_min_u32_e32 v134, v47, v134
	v_min_u32_e32 v143, v48, v143
	v_min_u32_e32 v149, v49, v149
	v_min_u32_e32 v50, v50, v150
	v_min_u32_e32 v51, v51, v151
	v_min_u32_e32 v52, v52, v152
	v_min_u32_e32 v53, v53, v153
	v_max_u32_e32 v48, v154, v50
	v_max_u32_e32 v49, v134, v51
	v_max_u32_e32 v97, v143, v52
	v_max_u32_e32 v151, v149, v53
	v_max_u32_e32 v46, v48, v97
	v_max_u32_e32 v150, v49, v151
	v_min_u32_e32 v97, v48, v97
	v_min_u32_e32 v49, v49, v151
	v_min_u32_e32 v47, v46, v150
	v_max_u32_e32 v48, v97, v49
	v_min_u32_e32 v49, v97, v49
	v_cmp_lt_i32_e32 vcc, 0, v1
	s_and_saveexec_b64 s[0:1], vcc
	s_xor_b64 s[0:1], exec, s[0:1]
	s_cbranch_execz .LBB0_675
	s_nop 1
	v_ashrrev_i32_e32 v97, 31, v47
	v_bitop3_b32 v97, v47, v97, s12 bitop3:0x93
	v_add_f32_e32 v97, v54, v97
	v_cmp_lt_i32_e32 vcc, -1, v97
	s_nop 1
	v_cndmask_b32_e32 v151, -1, v132, vcc
	v_bitop3_b32 v97, v151, s60, v97 bitop3:0x48
	v_or_b32_e32 v97, 0xf6, v97
	v_cmp_ne_u32_e32 vcc, 1, v1
	s_and_saveexec_b64 s[4:5], vcc
	s_cbranch_execz .LBB0_674
	v_and_b32_e32 v151, 0xffffff80, v48
	v_ashrrev_i32_e32 v152, 31, v49
	v_cmp_lt_i32_e32 vcc, -1, v48
	v_bitop3_b32 v153, v49, v152, s12 bitop3:0x93
	s_movk_i32 s6, 0xf4
	v_cndmask_b32_e64 v155, v132, -1, vcc
	v_xor_b32_e32 v152, v155, v151
	v_pk_add_f32 v[152:153], v[54:55], v[152:153] op_sel_hi:[0,1]
	v_cmp_lt_i32_e32 vcc, -1, v153
	v_and_b32_e32 v151, 0xffffff00, v153
	s_nop 0
	v_cndmask_b32_e32 v97, v133, v132, vcc
	v_cmp_lt_i32_e32 vcc, -1, v152
	v_bitop3_b32 v97, v97, s6, v151 bitop3:0xde
	v_and_b32_e32 v152, 0xffffff00, v152
	v_cndmask_b32_e32 v151, v133, v132, vcc
	s_movk_i32 s6, 0xf5
	v_bitop3_b32 v151, v151, s6, v152 bitop3:0xde
	v_cndmask_b32_e64 v97, v97, v151, s[38:39]

; __device__ __forceinline__ unsigned mono(float f) { const unsigned u = __float_as_uint(f); return (u & 0x80000000u) ? ~u : (u ^ 0x80000000u); }
; __device__ __forceinline__ float unmono(unsigned u) { return __uint_as_float((u & 0x80000000u) ? (u ^ 0x80000000u) : ~u); }
; __device__ __forceinline__ void topk_phase(LAS unsigned char* lds, const bf16_t* qp, const bf16_t* keys, const float* SU, const float* SV, int* sel_e, float* sel_g, float* sel_su, int G, int b) {
;     ...
;         for (int i = 0; i < 16; ++i) { v1[i] = unmono(T[0][i] & ~127u); v2[i] = unmono(T[1][i] & ~127u); }
;         unsigned ck[16];
; #pragma unroll
;         for (int sidx = 0; sidx < 13; ++sidx) {
;             unsigned keyk[4];
; #pragma unroll
;             for (int k = 0; k < 4; ++k) {
;                 const int c = 4 * sidx + k;
;                 if (c < 50) { const int ci = cand_i(c), cj = cand_j(c); keyk[k] = (mono(v1[ci] + v2[cj]) & ~255u) | (unsigned)(255 - (ci * 16 + cj)); }
;                 else keyk[k] = 0u;
;             }
;             ck[sidx] = fq == 0 ? keyk[0] : fq == 1 ? keyk[1] : fq == 2 ? keyk[2] : keyk[3];
;         }
.LBB0_675:
	s_or_saveexec_b64 s[0:1], s[0:1]
	v_max_u32_e32 v46, v46, v150
	s_xor_b64 exec, exec, s[0:1]
	s_nop 1
	v_ashrrev_i32_e32 v97, 31, v46
	v_bitop3_b32 v97, v46, v97, s12 bitop3:0x93
	v_add_f32_e32 v97, v54, v97
	v_cmp_lt_i32_e32 vcc, -1, v97
	s_nop 1
	v_cndmask_b32_e32 v150, -1, v132, vcc
	v_bitop3_b32 v97, v150, s60, v97 bitop3:0x48
	v_or_b32_e32 v97, 0xf7, v97
	s_or_b64 exec, exec, s[0:1]
	v_min_u32_e32 v150, v154, v50
	v_min_u32_e32 v134, v134, v51
	v_min_u32_e32 v52, v143, v52
	v_min_u32_e32 v53, v149, v53
	v_max_u32_e32 v50, v150, v52
	v_max_u32_e32 v143, v134, v53
	v_min_u32_e32 v149, v150, v52
	v_min_u32_e32 v53, v134, v53
	v_min_u32_e32 v51, v50, v143
	v_max_u32_e32 v52, v149, v53
	v_min_u32_e32 v53, v149, v53
	v_cmp_lt_i32_e32 vcc, 0, v1
	s_and_saveexec_b64 s[0:1], vcc
	s_xor_b64 s[0:1], exec, s[0:1]
	s_cbranch_execz .LBB0_681
	s_nop 1
	v_ashrrev_i32_e32 v134, 31, v51
	v_bitop3_b32 v134, v51, v134, s12 bitop3:0x93
	v_add_f32_e32 v134, v54, v134
	v_cmp_lt_i32_e32 vcc, -1, v134
	s_nop 1
	v_cndmask_b32_e32 v149, -1, v132, vcc
	v_bitop3_b32 v134, v149, s60, v134 bitop3:0x48
	v_or_b32_e32 v134, 0xf2, v134
	v_cmp_ne_u32_e32 vcc, 1, v1
	s_and_saveexec_b64 s[4:5], vcc
	s_cbranch_execz .LBB0_680
	v_and_b32_e32 v149, 0xffffff80, v52
	v_ashrrev_i32_e32 v150, 31, v53
	v_cmp_lt_i32_e32 vcc, -1, v52
	v_bitop3_b32 v151, v53, v150, s12 bitop3:0x93
	s_movk_i32 s6, 0xf0
	v_cndmask_b32_e64 v152, v132, -1, vcc
	v_xor_b32_e32 v150, v152, v149
	v_pk_add_f32 v[150:151], v[54:55], v[150:151] op_sel_hi:[0,1]
	v_cmp_lt_i32_e32 vcc, -1, v151
	v_and_b32_e32 v134, 0xffffff00, v151
	v_and_b32_e32 v149, 0xffffff00, v150
	v_cndmask_b32_e32 v54, v133, v132, vcc
	v_cmp_lt_i32_e32 vcc, -1, v150
	v_bitop3_b32 v54, v54, s6, v134 bitop3:0xde
	s_movk_i32 s6, 0xf1
	v_cndmask_b32_e32 v134, v133, v132, vcc
	v_bitop3_b32 v134, v134, s6, v149 bitop3:0xde
	v_cndmask_b32_e64 v134, v54, v134, s[38:39]

; __device__ __forceinline__ unsigned mono(float f) { const unsigned u = __float_as_uint(f); return (u & 0x80000000u) ? ~u : (u ^ 0x80000000u); }
; __device__ __forceinline__ float unmono(unsigned u) { return __uint_as_float((u & 0x80000000u) ? (u ^ 0x80000000u) : ~u); }
; __device__ __forceinline__ void topk_phase(LAS unsigned char* lds, const bf16_t* qp, const bf16_t* keys, const float* SU, const float* SV, int* sel_e, float* sel_g, float* sel_su, int G, int b) {
;     ...
;         for (int i = 0; i < 16; ++i) { v1[i] = unmono(T[0][i] & ~127u); v2[i] = unmono(T[1][i] & ~127u); }
;         unsigned ck[16];
; #pragma unroll
;         for (int sidx = 0; sidx < 13; ++sidx) {
;             unsigned keyk[4];
; #pragma unroll
;             for (int k = 0; k < 4; ++k) {
;                 const int c = 4 * sidx + k;
;                 if (c < 50) { const int ci = cand_i(c), cj = cand_j(c); keyk[k] = (mono(v1[ci] + v2[cj]) & ~255u) | (unsigned)(255 - (ci * 16 + cj)); }
;                 else keyk[k] = 0u;
;             }
;             ck[sidx] = fq == 0 ? keyk[0] : fq == 1 ? keyk[1] : fq == 2 ? keyk[2] : keyk[3];
;         }
.LBB0_681:
	s_or_saveexec_b64 s[0:1], s[0:1]
	v_max_u32_e32 v50, v50, v143
	s_xor_b64 exec, exec, s[0:1]
	s_nop 1
	v_ashrrev_i32_e32 v134, 31, v50
	v_bitop3_b32 v134, v50, v134, s12 bitop3:0x93
	v_add_f32_e32 v54, v54, v134
	v_cmp_lt_i32_e32 vcc, -1, v54
	s_nop 1
	v_cndmask_b32_e32 v134, -1, v132, vcc
	v_bitop3_b32 v54, v134, s60, v54 bitop3:0x48
	v_or_b32_e32 v134, 0xf3, v54
	s_or_b64 exec, exec, s[0:1]
	v_min_u32_e32 v35, v35, v142
	s_nop 1
	v_ashrrev_i32_e32 v54, 31, v35
	v_bitop3_b32 v54, v35, v54, s12 bitop3:0x93
	v_cmp_lt_i32_e32 vcc, 0, v1
	s_and_saveexec_b64 s[0:1], vcc
	s_xor_b64 s[0:1], exec, s[0:1]
	s_cbranch_execz .LBB0_687
	v_add_f32_e32 v142, v67, v54
	v_cmp_lt_i32_e32 vcc, -1, v142
	s_nop 1
	v_cndmask_b32_e32 v143, -1, v132, vcc
	v_bitop3_b32 v142, v143, s60, v142 bitop3:0x48
	v_or_b32_e32 v142, 0xee, v142
	v_cmp_ne_u32_e32 vcc, 1, v1
	s_and_saveexec_b64 s[4:5], vcc
	s_cbranch_execz .LBB0_686
	v_pk_add_f32 v[142:143], v[54:55], v[56:57] op_sel_hi:[0,1]
	v_cmp_lt_i32_e32 vcc, -1, v143
	v_and_b32_e32 v143, 0xffffff00, v143
	s_movk_i32 s6, 0xec
	v_cndmask_b32_e32 v149, v133, v132, vcc
	v_cmp_lt_i32_e32 vcc, -1, v142
	v_bitop3_b32 v143, v149, s6, v143 bitop3:0xde
	v_and_b32_e32 v142, 0xffffff00, v142
	v_cndmask_b32_e32 v149, v133, v132, vcc
	s_movk_i32 s6, 0xed
	v_bitop3_b32 v142, v149, s6, v142 bitop3:0xde
	v_cndmask_b32_e64 v142, v143, v142, s[38:39]

; __device__ __forceinline__ unsigned mono(float f) { const unsigned u = __float_as_uint(f); return (u & 0x80000000u) ? ~u : (u ^ 0x80000000u); }
; __device__ __forceinline__ float unmono(unsigned u) { return __uint_as_float((u & 0x80000000u) ? (u ^ 0x80000000u) : ~u); }
; __device__ __forceinline__ void topk_phase(LAS unsigned char* lds, const bf16_t* qp, const bf16_t* keys, const float* SU, const float* SV, int* sel_e, float* sel_g, float* sel_su, int G, int b) {
;     ...
;         for (int i = 0; i < 16; ++i) { v1[i] = unmono(T[0][i] & ~127u); v2[i] = unmono(T[1][i] & ~127u); }
;         unsigned ck[16];
; #pragma unroll
;         for (int sidx = 0; sidx < 13; ++sidx) {
;             unsigned keyk[4];
; #pragma unroll
;             for (int k = 0; k < 4; ++k) {
;                 const int c = 4 * sidx + k;
;                 if (c < 50) { const int ci = cand_i(c), cj = cand_j(c); keyk[k] = (mono(v1[ci] + v2[cj]) & ~255u) | (unsigned)(255 - (ci * 16 + cj)); }
;                 else keyk[k] = 0u;
;             }
;             ck[sidx] = fq == 0 ? keyk[0] : fq == 1 ? keyk[1] : fq == 2 ? keyk[2] : keyk[3];
;         }
.LBB0_693:
	s_andn2_saveexec_b64 s[0:1], s[0:1]
	v_add_f32_e32 v36, v54, v147
	v_cmp_lt_i32_e32 vcc, -1, v36
	s_nop 1
	v_cndmask_b32_e32 v37, -1, v132, vcc
	v_bitop3_b32 v36, v37, s60, v36 bitop3:0x48
	v_or_b32_e32 v143, 0xeb, v36
	s_or_b64 exec, exec, s[0:1]
	v_min_u32_e32 v37, v58, v145
	v_min_u32_e32 v58, v144, v146
	v_max_u32_e32 v36, v37, v58
	s_nop 1
	v_ashrrev_i32_e32 v54, 31, v36
	v_bitop3_b32 v54, v36, v54, s12 bitop3:0x93
	v_cmp_lt_i32_e32 vcc, 0, v1
	s_and_saveexec_b64 s[0:1], vcc
	s_xor_b64 s[0:1], exec, s[0:1]
	s_cbranch_execz .LBB0_699
	v_add_f32_e32 v144, v67, v54
	v_cmp_lt_i32_e32 vcc, -1, v144
	s_nop 1
	v_cndmask_b32_e32 v145, -1, v132, vcc
	v_bitop3_b32 v144, v145, s60, v144 bitop3:0x48
	v_or_b32_e32 v144, 0xde, v144
	v_cmp_ne_u32_e32 vcc, 1, v1
	s_and_saveexec_b64 s[4:5], vcc
	s_cbranch_execz .LBB0_698
	v_pk_add_f32 v[144:145], v[54:55], v[56:57] op_sel_hi:[0,1]
	v_cmp_lt_i32_e32 vcc, -1, v145
	v_and_b32_e32 v145, 0xffffff00, v145
	s_movk_i32 s6, 0xdc
	v_cndmask_b32_e32 v146, v133, v132, vcc
	v_cmp_lt_i32_e32 vcc, -1, v144
	v_bitop3_b32 v145, v146, s6, v145 bitop3:0xde
	v_and_b32_e32 v144, 0xffffff00, v144
	v_cndmask_b32_e32 v146, v133, v132, vcc
	s_movk_i32 s6, 0xdd
	v_bitop3_b32 v144, v146, s6, v144 bitop3:0xde
	v_cndmask_b32_e64 v144, v145, v144, s[38:39]

; __device__ __forceinline__ unsigned mono(float f) { const unsigned u = __float_as_uint(f); return (u & 0x80000000u) ? ~u : (u ^ 0x80000000u); }
; __device__ __forceinline__ float unmono(unsigned u) { return __uint_as_float((u & 0x80000000u) ? (u ^ 0x80000000u) : ~u); }
; __device__ __forceinline__ void topk_phase(LAS unsigned char* lds, const bf16_t* qp, const bf16_t* keys, const float* SU, const float* SV, int* sel_e, float* sel_g, float* sel_su, int G, int b) {
;     ...
;         for (int i = 0; i < 16; ++i) { v1[i] = unmono(T[0][i] & ~127u); v2[i] = unmono(T[1][i] & ~127u); }
;         unsigned ck[16];
; #pragma unroll
;         for (int sidx = 0; sidx < 13; ++sidx) {
;             unsigned keyk[4];
; #pragma unroll
;             for (int k = 0; k < 4; ++k) {
;                 const int c = 4 * sidx + k;
;                 if (c < 50) { const int ci = cand_i(c), cj = cand_j(c); keyk[k] = (mono(v1[ci] + v2[cj]) & ~255u) | (unsigned)(255 - (ci * 16 + cj)); }
;                 else keyk[k] = 0u;
;             }
;             ck[sidx] = fq == 0 ? keyk[0] : fq == 1 ? keyk[1] : fq == 2 ? keyk[2] : keyk[3];
;         }
.LBB0_699:
	s_andn2_saveexec_b64 s[0:1], s[0:1]
	v_add_f32_e32 v144, v66, v54
	v_cmp_lt_i32_e32 vcc, -1, v144
	s_nop 1
	v_cndmask_b32_e32 v145, -1, v132, vcc
	v_bitop3_b32 v144, v145, s60, v144 bitop3:0x48
	v_or_b32_e32 v144, 0xdf, v144
	s_or_b64 exec, exec, s[0:1]
	v_min_u32_e32 v37, v37, v58
	s_nop 1
	v_ashrrev_i32_e32 v58, 31, v37
	v_bitop3_b32 v58, v37, v58, s12 bitop3:0x93
	v_cmp_lt_i32_e32 vcc, 0, v1
	s_and_saveexec_b64 s[0:1], vcc
	s_xor_b64 s[0:1], exec, s[0:1]
	s_cbranch_execz .LBB0_705
	v_add_f32_e32 v54, v66, v58
	v_cmp_lt_i32_e32 vcc, -1, v54
	s_nop 1
	v_cndmask_b32_e32 v145, -1, v132, vcc
	v_bitop3_b32 v54, v145, s60, v54 bitop3:0x48
	v_or_b32_e32 v145, 0xcf, v54
	v_cmp_ne_u32_e32 vcc, 1, v1
	s_and_saveexec_b64 s[4:5], vcc
	s_cbranch_execz .LBB0_704
	v_pk_mov_b32 v[146:147], v[66:67], v[56:57] op_sel:[1,0]
	s_movk_i32 s6, 0xcd
	v_pk_add_f32 v[146:147], v[58:59], v[146:147] op_sel_hi:[0,1]
	v_cmp_lt_i32_e32 vcc, -1, v147
	v_and_b32_e32 v145, 0xffffff00, v147
	s_nop 0
	v_cndmask_b32_e32 v54, v133, v132, vcc
	v_cmp_lt_i32_e32 vcc, -1, v146
	v_bitop3_b32 v54, v54, s6, v145 bitop3:0xde
	v_and_b32_e32 v146, 0xffffff00, v146
	v_cndmask_b32_e32 v145, v133, v132, vcc
	s_movk_i32 s6, 0xce
	v_bitop3_b32 v145, v145, s6, v146 bitop3:0xde
	v_cndmask_b32_e64 v145, v54, v145, s[38:39]

; __device__ __forceinline__ unsigned mono(float f) { const unsigned u = __float_as_uint(f); return (u & 0x80000000u) ? ~u : (u ^ 0x80000000u); }
; __device__ __forceinline__ float unmono(unsigned u) { return __uint_as_float((u & 0x80000000u) ? (u ^ 0x80000000u) : ~u); }
; __device__ __forceinline__ void topk_phase(LAS unsigned char* lds, const bf16_t* qp, const bf16_t* keys, const float* SU, const float* SV, int* sel_e, float* sel_g, float* sel_su, int G, int b) {
;     ...
;             TOPK_XMERGE(T[p], 16); TOPK_XMERGE(T[p], 32);
;         }
;         float v1[16], v2[16];
; #pragma unroll
;         for (int i = 0; i < 16; ++i) { v1[i] = unmono(T[0][i] & ~127u); v2[i] = unmono(T[1][i] & ~127u); }
;         unsigned ck[16];
; #pragma unroll
;         for (int sidx = 0; sidx < 13; ++sidx) {
;             unsigned keyk[4];
; #pragma unroll
;             for (int k = 0; k < 4; ++k) {
;                 const int c = 4 * sidx + k;
;                 if (c < 50) { const int ci = cand_i(c), cj = cand_j(c); keyk[k] = (mono(v1[ci] + v2[cj]) & ~255u) | (unsigned)(255 - (ci * 16 + cj)); }
;                 else keyk[k] = 0u;
;             }
;             ck[sidx] = fq == 0 ? keyk[0] : fq == 1 ? keyk[1] : fq == 2 ? keyk[2] : keyk[3];
;         }
.LBB0_717:
	s_andn2_saveexec_b64 s[0:1], s[0:1]
	v_add_f32_e32 v136, v66, v140
	v_cmp_lt_i32_e32 vcc, -1, v136
	s_nop 1
	v_cndmask_b32_e32 v137, -1, v132, vcc
	v_bitop3_b32 v136, v137, s60, v136 bitop3:0x48
	v_or_b32_e32 v136, 0xaf, v136
	s_or_b64 exec, exec, s[0:1]
	v_min_u32_e32 v57, v57, v58
	v_min_u32_e32 v71, v59, v71
	v_min_u32_e32 v60, v60, v72
	v_min_u32_e32 v72, v61, v73
	v_min_u32_e32 v62, v62, v74
	v_min_u32_e32 v63, v63, v75
	v_min_u32_e32 v64, v64, v76
	v_min_u32_e32 v65, v65, v77
	v_min_u32_e32 v73, v70, v96
	v_max_u32_e32 v61, v71, v63
	v_max_u32_e32 v74, v60, v64
	v_max_u32_e32 v75, v72, v65
	v_max_u32_e32 v76, v62, v73
	v_ashrrev_i32_e32 v58, 31, v57
	v_max_u32_e32 v59, v61, v75
	v_max_u32_e32 v70, v74, v76
	v_bitop3_b32 v137, v57, v58, s12 bitop3:0x93
	v_max_u32_e32 v58, v59, v70
	v_min_u32_e32 v59, v59, v70
	v_cmp_lt_i32_e32 vcc, 0, v1
	s_and_saveexec_b64 s[0:1], vcc
	s_xor_b64 s[0:1], exec, s[0:1]
	s_cbranch_execz .LBB0_723
	v_add_f32_e32 v70, v67, v137
	v_cmp_lt_i32_e32 vcc, -1, v70
	s_nop 1
	v_cndmask_b32_e32 v77, -1, v132, vcc
	v_bitop3_b32 v70, v77, s60, v70 bitop3:0x48
	v_or_b32_e32 v70, 0x8e, v70
	v_cmp_ne_u32_e32 vcc, 1, v1
	s_and_saveexec_b64 s[4:5], vcc
	s_cbranch_execz .LBB0_722
	v_and_b32_e32 v77, 0xffffff80, v58
	v_ashrrev_i32_e32 v96, 31, v59
	v_cmp_lt_i32_e32 vcc, -1, v58
	v_bitop3_b32 v139, v59, v96, s12 bitop3:0x93
	s_movk_i32 s6, 0x6f
	v_cndmask_b32_e64 v137, v132, -1, vcc
	v_xor_b32_e32 v138, v137, v77
	v_pk_add_f32 v[138:139], v[66:67], v[138:139] op_sel_hi:[0,1]
	v_cmp_lt_i32_e32 vcc, -1, v139
	v_and_b32_e32 v77, 0xffffff00, v139
	v_and_b32_e32 v96, 0xffffff00, v138
	v_cndmask_b32_e32 v70, v133, v132, vcc
	v_cmp_lt_i32_e32 vcc, -1, v138
	v_bitop3_b32 v70, v70, s6, v77 bitop3:0xde
	s_movk_i32 s6, 0x7f
	v_cndmask_b32_e32 v77, v133, v132, vcc
	v_bitop3_b32 v77, v77, s6, v96 bitop3:0xde
	v_cndmask_b32_e64 v70, v70, v77, s[38:39]
